# rwkv chunk phase (p5): loop-header vmcnt waits no longer force the previous item's 12 output stores (counts +12, 12 dummy loads in preheader keep entry state identical)
# baseline (speedup 1.0000x reference)
.LBB0_1216:
	s_or_b64 exec, exec, s[4:5]
	s_cmpk_lt_i32 s96, 0x1000
	s_cselect_b64 s[2:3], -1, 0
	v_readfirstlane_b32 s1, v2
	v_writelane_b32 v232, s2, 39
	s_cmpk_gt_i32 s96, 0xfff
	s_nop 0
	v_writelane_b32 v232, s3, 40
	s_cbranch_scc1 .LBB0_1228
	s_ashr_i32 s48, s1, 8
	s_mul_i32 s0, s48, 0xfe00
	s_lshl_b32 s4, s16, 10
	s_add_i32 s0, s0, 0
	s_lshl_b32 s8, s16, 9
	s_ashr_i32 s5, s4, 31
	s_lshr_b32 s2, s1, 6
	s_bfe_u32 s49, s1, 0x20006
	s_add_i32 s50, s0, 0xb400
	s_add_i32 s51, s0, 0xdc00
	s_ashr_i32 s9, s8, 31
	s_lshl_b64 s[6:7], s[4:5], 2
	v_readlane_b32 s12, v233, 36
	v_readlane_b32 s13, v233, 37
	s_add_u32 s4, s12, s6
	v_readlane_b32 s16, v233, 40
	s_addc_u32 s5, s13, s7
	v_readlane_b32 s17, v233, 41
	s_add_u32 s6, s16, s6
	v_readlane_b32 s22, v233, 46
	s_addc_u32 s7, s17, s7
	s_lshl_b64 s[8:9], s[8:9], 2
	v_readlane_b32 s23, v233, 47
	s_add_u32 s28, s22, s8
	v_readlane_b32 s24, v233, 48
	s_addc_u32 s29, s23, s9
	v_readlane_b32 s25, v233, 49
	s_add_u32 s30, s24, s8
	s_addc_u32 s31, s25, s9
	s_add_u32 s34, s44, 0x2b400000
	s_addc_u32 s35, s45, 0
	s_add_u32 s36, s44, 0x2c400000
	s_addc_u32 s37, s45, 0
	s_add_u32 s38, s44, 0x2d400000
	s_addc_u32 s39, s45, 0
	s_add_u32 s40, s44, 0x30400000
	s_addc_u32 s41, s45, 0
	s_add_u32 s42, s44, 0x31400000
	s_addc_u32 s43, s45, 0
	s_bfe_u32 s54, s2, 0x10001
	s_add_i32 s2, s48, s62
	s_ashr_i32 s3, s2, 31
	s_lshr_b32 s3, s3, 25
	s_add_i32 s3, s2, s3
	s_ashr_i32 s8, s3, 7
	s_and_b32 s3, s3, 0x7ffff80
	s_sub_i32 s2, s2, s3
	s_lshl_b32 s9, s8, 8
	s_and_b32 s3, s8, 1
	s_and_b32 s9, s9, 0x7ff000
	s_lshl_b32 s2, s2, 5
	s_lshl_b32 s8, s8, 5
	s_add_i32 s9, s9, s2
	s_lshl_b32 s2, s3, 9
	s_and_b32 s8, s8, 0x1c0
	v_and_b32_e32 v33, 63, v2
	s_or_b32 s2, s2, s8
	v_bfe_u32 v3, v2, 6, 2
	s_bfe_u32 s55, s1, 0x10006
	s_add_i32 s1, s0, 0x3600
	v_or_b32_e32 v1, s2, v33
	v_lshlrev_b32_e32 v1, 2, v1
	v_or_b32_e32 v41, s8, v33
	v_lshlrev_b32_e32 v49, 3, v3
	s_cmp_eq_u32 s3, 0
	global_load_dword v59, v1, s[4:5]
	global_load_dword v60, v1, s[6:7]
	v_lshlrev_b32_e32 v1, 2, v41
	v_xor_b32_e32 v58, 31, v49
	s_cselect_b64 vcc, -1, 0
	global_load_dword v16, v1, s[30:31]
	global_load_dword v18, v1, s[28:29]
	v_cndmask_b32_e32 v1, v58, v49, vcc
	v_or_b32_e32 v1, s9, v1
	v_or_b32_e32 v61, 1, v49
	v_xor_b32_e32 v62, 30, v49
	v_lshl_or_b32 v14, v1, 9, v41
	v_cndmask_b32_e32 v1, v62, v61, vcc
	v_mov_b32_e32 v15, 0
	v_or_b32_e32 v1, s9, v1
	v_lshlrev_b64 v[4:5], 1, v[14:15]
	v_lshl_or_b32 v14, v1, 9, v41
	v_lshl_add_u64 v[6:7], s[36:37], 0, v[4:5]
	v_lshl_add_u64 v[8:9], s[40:41], 0, v[4:5]
	v_lshlrev_b64 v[24:25], 1, v[14:15]
	v_or_b32_e32 v63, 2, v49
	v_xor_b32_e32 v64, 29, v49
	v_lshl_add_u64 v[10:11], s[42:43], 0, v[4:5]
	v_lshl_add_u64 v[12:13], s[34:35], 0, v[4:5]
	v_lshl_add_u64 v[4:5], s[38:39], 0, v[4:5]
	v_lshl_add_u64 v[26:27], s[36:37], 0, v[24:25]
	v_lshl_add_u64 v[28:29], s[40:41], 0, v[24:25]
	v_lshl_add_u64 v[30:31], s[42:43], 0, v[24:25]
	global_load_ushort v20, v[6:7], off
	global_load_ushort v67, v[8:9], off
	global_load_ushort v68, v[10:11], off
	global_load_ushort v22, v[12:13], off
	global_load_ushort v69, v[4:5], off
	global_load_ushort v1, v[26:27], off
	global_load_ushort v72, v[28:29], off
	global_load_ushort v75, v[30:31], off
	v_cndmask_b32_e32 v8, v64, v63, vcc
	v_or_b32_e32 v8, s9, v8
	v_lshl_or_b32 v14, v8, 9, v41
	v_or_b32_e32 v65, 3, v49
	v_xor_b32_e32 v66, 28, v49
	v_lshlrev_b64 v[8:9], 1, v[14:15]
	v_cndmask_b32_e32 v14, v66, v65, vcc
	v_or_b32_e32 v14, s9, v14
	v_lshl_or_b32 v14, v14, 9, v41
	v_lshl_add_u64 v[4:5], s[34:35], 0, v[24:25]
	v_lshl_add_u64 v[12:13], s[40:41], 0, v[8:9]
	v_lshl_add_u64 v[28:29], s[34:35], 0, v[8:9]
	v_lshlrev_b64 v[30:31], 1, v[14:15]
	v_or_b32_e32 v70, 4, v49
	v_xor_b32_e32 v71, 27, v49
	v_lshl_add_u64 v[6:7], s[38:39], 0, v[24:25]
	v_lshl_add_u64 v[10:11], s[36:37], 0, v[8:9]
	v_lshl_add_u64 v[26:27], s[42:43], 0, v[8:9]
	v_lshl_add_u64 v[8:9], s[38:39], 0, v[8:9]
	v_lshl_add_u64 v[34:35], s[36:37], 0, v[30:31]
	global_load_ushort v17, v[4:5], off
	global_load_ushort v80, v[6:7], off
	global_load_ushort v24, v[10:11], off
	global_load_ushort v81, v[12:13], off
	global_load_ushort v84, v[26:27], off
	s_nop 0
	global_load_ushort v28, v[28:29], off
	s_nop 0
	global_load_ushort v85, v[8:9], off
	global_load_ushort v19, v[34:35], off
	v_cndmask_b32_e32 v12, v71, v70, vcc
	v_or_b32_e32 v12, s9, v12
	v_lshl_or_b32 v14, v12, 9, v41
	v_lshl_add_u64 v[4:5], s[40:41], 0, v[30:31]
	v_lshl_add_u64 v[6:7], s[42:43], 0, v[30:31]
	v_lshlrev_b64 v[12:13], 1, v[14:15]
	v_or_b32_e32 v73, 5, v49
	v_xor_b32_e32 v74, 26, v49
	v_lshl_add_u64 v[8:9], s[34:35], 0, v[30:31]
	v_lshl_add_u64 v[10:11], s[38:39], 0, v[30:31]
	v_lshl_add_u64 v[26:27], s[36:37], 0, v[12:13]
	v_lshl_add_u64 v[34:35], s[40:41], 0, v[12:13]
	v_lshl_add_u64 v[36:37], s[42:43], 0, v[12:13]
	v_lshl_add_u64 v[38:39], s[34:35], 0, v[12:13]
	global_load_ushort v86, v[4:5], off
	global_load_ushort v87, v[6:7], off
	global_load_ushort v21, v[8:9], off
	global_load_ushort v88, v[10:11], off
	global_load_ushort v30, v[26:27], off
	global_load_ushort v96, v[34:35], off
	global_load_ushort v100, v[36:37], off
	global_load_ushort v32, v[38:39], off
	v_cndmask_b32_e32 v6, v74, v73, vcc
	v_or_b32_e32 v6, s9, v6
	v_lshl_or_b32 v14, v6, 9, v41
	v_or_b32_e32 v76, 6, v49
	v_xor_b32_e32 v77, 25, v49
	v_lshlrev_b64 v[6:7], 1, v[14:15]
	v_cndmask_b32_e32 v14, v77, v76, vcc
	v_or_b32_e32 v14, s9, v14
	v_lshl_or_b32 v14, v14, 9, v41
	v_lshl_add_u64 v[4:5], s[38:39], 0, v[12:13]
	v_lshl_add_u64 v[10:11], s[40:41], 0, v[6:7]
	v_lshlrev_b64 v[34:35], 1, v[14:15]
	v_or_b32_e32 v78, 7, v49
	v_xor_b32_e32 v79, 24, v49
	v_lshl_add_u64 v[8:9], s[36:37], 0, v[6:7]
	v_lshl_add_u64 v[12:13], s[42:43], 0, v[6:7]
	v_lshl_add_u64 v[26:27], s[34:35], 0, v[6:7]
	v_lshl_add_u64 v[6:7], s[38:39], 0, v[6:7]
	v_lshl_add_u64 v[36:37], s[36:37], 0, v[34:35]
	v_lshl_add_u64 v[38:39], s[40:41], 0, v[34:35]
	global_load_ushort v107, v[4:5], off
	global_load_ushort v23, v[8:9], off
	global_load_ushort v113, v[10:11], off
	global_load_ushort v114, v[12:13], off
	global_load_ushort v25, v[26:27], off
	global_load_ushort v118, v[6:7], off
	global_load_ushort v46, v[36:37], off
	global_load_ushort v127, v[38:39], off
	v_cndmask_b32_e32 v10, v79, v78, vcc
	v_or_b32_e32 v10, s9, v10
	v_lshl_or_b32 v14, v10, 9, v41
	v_lshl_add_u64 v[4:5], s[42:43], 0, v[34:35]
	v_lshlrev_b64 v[10:11], 1, v[14:15]
	v_lshl_add_u64 v[6:7], s[34:35], 0, v[34:35]
	v_lshl_add_u64 v[8:9], s[38:39], 0, v[34:35]
	v_lshl_add_u64 v[12:13], s[36:37], 0, v[10:11]
	v_lshl_add_u64 v[26:27], s[40:41], 0, v[10:11]
	v_lshl_add_u64 v[34:35], s[42:43], 0, v[10:11]
	v_lshl_add_u64 v[36:37], s[34:35], 0, v[10:11]
	v_lshl_add_u64 v[10:11], s[38:39], 0, v[10:11]
	global_load_ushort v128, v[4:5], off
	global_load_ushort v48, v[6:7], off
	global_load_ushort v129, v[8:9], off
	global_load_ushort v29, v[12:13], off
	global_load_ushort v130, v[26:27], off
	global_load_ushort v131, v[34:35], off
	global_load_ushort v31, v[36:37], off
	global_load_ushort v132, v[10:11], off
	v_and_b32_e32 v4, 0xff, v2
	v_lshlrev_b32_e32 v14, 2, v33
	v_bfe_u32 v40, v2, 4, 2
	v_lshl_add_u32 v82, v4, 2, s0
	v_lshl_add_u64 v[4:5], s[44:45], 0, v[14:15]
	s_mov_b64 s[10:11], 0x3ea00000
	v_and_b32_e32 v47, 15, v2
	v_lshl_add_u64 v[26:27], v[4:5], 0, s[10:11]
	v_lshlrev_b32_e32 v4, 2, v40
	s_lshl_b32 s52, s90, 1
	v_cmp_le_u32_e32 vcc, v47, v4
	s_cmp_gt_u32 s49, 1
	s_movk_i32 s2, 0x1200
	v_cndmask_b32_e64 v5, 0, 1, vcc
	v_cmp_lt_u32_e32 vcc, v47, v4
	v_lshlrev_b32_e32 v11, 3, v40
	v_bfe_u32 v12, v2, 2, 2
	v_cndmask_b32_e64 v7, 0, 1, vcc
	s_cselect_b64 vcc, -1, 0
	s_and_b64 s[10:11], vcc, exec
	s_cselect_b32 s1, s1, s0
	s_cmp_eq_u32 s55, 0
	s_cselect_b32 s2, s2, 0x2400
	s_add_i32 s2, s0, s2
	v_cndmask_b32_e32 v5, v7, v5, vcc
	s_cmp_eq_u32 s49, 2
	s_mov_b32 s3, 0xe600
	v_and_b32_e32 v7, 48, v2
	v_or_b32_e32 v12, v11, v12
	v_lshlrev_b32_e32 v2, 3, v2
	s_cselect_b32 s3, s3, 0xf000
	v_add_u32_e32 v8, s1, v7
	v_mul_u32_u24_e32 v13, 40, v12
	s_lshl_b32 s1, s55, 5
	v_and_b32_e32 v2, 24, v2
	v_mul_u32_u24_e32 v12, 0x90, v12
	v_lshl_add_u32 v6, v47, 1, s0
	s_add_i32 s53, s0, s3
	v_lshlrev_b32_e32 v13, 1, v13
	s_add_i32 s3, s1, s0
	v_add3_u32 v92, s0, v12, v2
	v_add3_u32 v89, v13, s3, v2
	v_add_u32_e32 v13, s1, v6
	v_add_u32_e32 v93, 0x240, v92
	s_lshl_b32 s1, s49, 5
	v_readlane_b32 s14, v233, 38
	v_readlane_b32 s15, v233, 39
	v_add_u32_e32 v9, s2, v7
	s_lshl_b32 s2, s54, 4
	v_add_u32_e32 v94, s1, v92
	v_add_u32_e32 v95, s1, v93
	s_lshl_b32 s10, s55, 3
	s_add_i32 s1, s0, s1
	v_and_b32_e32 v5, 1, v5
	v_cmp_eq_u32_e64 s[8:9], 0, v3
	s_add_u32 s46, s44, s10
	v_cmp_lt_u32_e64 s[10:11], 1, v3
	v_cmp_eq_u32_e64 s[12:13], 3, v3
	v_mul_u32_u24_e32 v3, 0x240, v3
	v_cmp_eq_u32_e64 s[14:15], 1, v5
	v_cndmask_b32_e64 v5, 0, 1, vcc
	v_or_b32_e32 v10, s2, v47
	v_add_u32_e32 v11, s1, v11
	v_or_b32_e32 v3, v3, v33
	s_movk_i32 s1, 0x48
	v_or_b32_e32 v5, v4, v5
	v_mul_u32_u24_e32 v10, 40, v10
	v_lshl_or_b32 v36, s55, 4, v47
	v_lshl_add_u32 v101, v3, 1, s0
	v_mad_u32_u24 v3, v63, s1, v33
	v_cmp_gt_u32_e64 s[16:17], v47, v5
	v_or_b32_e32 v5, 2, v4
	v_add_u32_e32 v83, s0, v14
	v_lshl_add_u32 v10, v10, 1, s0
	v_lshl_add_u32 v91, v36, 1, s0
	v_add_u32_e32 v2, s0, v7
	v_lshl_add_u32 v102, v3, 1, s0
	v_cmp_le_u32_e64 s[0:1], v47, v5
	v_xor_b32_e32 v98, 64, v14
	v_xor_b32_e32 v99, 0x80, v14
	v_cndmask_b32_e64 v14, 0, 1, s[0:1]
	v_cmp_lt_u32_e64 s[0:1], v47, v5
	v_readlane_b32 s18, v233, 42
	v_readlane_b32 s19, v233, 43
	v_cndmask_b32_e64 v5, 0, 1, s[0:1]
	v_cndmask_b32_e32 v5, v5, v14, vcc
	v_and_b32_e32 v5, 1, v5
	v_cmp_eq_u32_e64 s[18:19], 1, v5
	v_or_b32_e32 v5, 3, v4
	v_cmp_le_u32_e64 s[0:1], v47, v5
	v_readlane_b32 s20, v233, 44
	v_readlane_b32 s21, v233, 45
	v_cndmask_b32_e64 v14, 0, 1, s[0:1]
	v_cmp_lt_u32_e64 s[0:1], v47, v5
	v_or_b32_e32 v3, 16, v47
	v_or_b32_e32 v34, 19, v4
	v_cndmask_b32_e64 v5, 0, 1, s[0:1]
	v_cndmask_b32_e32 v5, v5, v14, vcc
	v_and_b32_e32 v5, 1, v5
	v_cmp_eq_u32_e64 s[20:21], 1, v5
	v_or_b32_e32 v5, 17, v4
	v_cmp_le_u32_e64 s[0:1], v3, v5
	v_or_b32_e32 v14, 18, v4
	v_readlane_b32 s26, v233, 50
	v_cndmask_b32_e64 v35, 0, 1, s[0:1]
	v_cmp_lt_u32_e64 s[0:1], v3, v5
	v_readlane_b32 s27, v233, 51
	v_or_b32_e32 v4, s2, v4
	v_cndmask_b32_e64 v5, 0, 1, s[0:1]
	v_cndmask_b32_e32 v5, v5, v35, vcc
	v_and_b32_e32 v5, 1, v5
	v_cmp_le_u32_e64 s[0:1], v3, v14
	v_cmp_eq_u32_e64 s[22:23], 1, v5
	s_movk_i32 s3, 0x90
	v_cndmask_b32_e64 v5, 0, 1, s[0:1]
	v_cmp_lt_u32_e64 s[0:1], v3, v14
	v_mul_u32_u24_e32 v50, 0x90, v4
	v_mul_u32_u24_e32 v51, 0x50, v4
	v_cndmask_b32_e64 v14, 0, 1, s[0:1]
	v_cndmask_b32_e32 v5, v14, v5, vcc
	v_and_b32_e32 v5, 1, v5
	v_cmp_le_u32_e64 s[0:1], v3, v34
	v_cmp_eq_u32_e64 s[24:25], 1, v5
	s_addc_u32 s47, s45, 0
	v_cndmask_b32_e64 v5, 0, 1, s[0:1]
	v_cmp_lt_u32_e64 s[0:1], v3, v34
	v_mul_u32_u24_e32 v12, 40, v47
	v_mul_u32_u24_e32 v3, 40, v3
	v_cndmask_b32_e64 v14, 0, 1, s[0:1]
	v_cndmask_b32_e32 v5, v14, v5, vcc
	v_and_b32_e32 v5, 1, v5
	v_cmp_eq_u32_e64 s[26:27], 1, v5
	v_mul_u32_u24_e32 v5, 40, v4
	v_lshl_add_u32 v106, v5, 1, v13
	v_or_b32_e32 v5, 1, v4
	v_cmp_eq_u32_e32 vcc, v4, v36
	s_movk_i32 s0, 0x50
	v_lshl_add_u32 v97, v12, 1, v2
	v_cndmask_b32_e64 v34, 0, 1.0, vcc
	v_cmp_eq_u32_e32 vcc, v5, v36
	v_or_b32_e32 v5, 3, v4
	v_or_b32_e32 v4, 2, v4
	v_cndmask_b32_e64 v35, 0, 1.0, vcc
	v_mul_lo_u32 v111, v5, s0
	v_mul_lo_u32 v52, v5, s3
	v_cmp_eq_u32_e32 vcc, v5, v36
	v_lshlrev_b32_e32 v5, 3, v33
	v_mul_lo_u32 v109, v4, s0
	s_lshl_b32 s0, s55, 6
	v_lshl_or_b32 v14, s49, 11, v5
	v_add_u32_e32 v110, v13, v109
	v_add_u32_e32 v112, v13, v111
	v_mul_lo_u32 v13, v4, s3
	v_cndmask_b32_e64 v37, 0, 1.0, vcc
	v_cmp_eq_u32_e32 vcc, v4, v36
	v_add_u32_e32 v115, s0, v92
	v_add_u32_e32 v116, s0, v93
	v_add_u32_e32 v4, s0, v6
	v_lshl_add_u32 v117, v3, 1, v2
	v_lshl_add_u64 v[2:3], s[44:45], 0, v[14:15]
	s_mov_b64 s[0:1], 0x8400000
	v_lshl_or_b32 v14, s49, 9, v5
	v_lshl_add_u64 v[38:39], v[2:3], 0, s[0:1]
	v_lshl_add_u64 v[2:3], s[44:45], 0, v[14:15]
	s_mov_b64 s[0:1], 0xc400000
	v_mul_u32_u24_e32 v105, 0x140, v40
	v_lshl_add_u64 v[40:41], v[2:3], 0, s[0:1]
	v_lshlrev_b32_e32 v2, 4, v33
	v_lshl_or_b32 v14, s54, 10, v2
	v_lshl_add_u64 v[2:3], s[46:47], 0, v[14:15]
	s_mov_b64 s[0:1], 0x4400000
	v_mul_u32_u24_e32 v12, 0x90, v47
	v_lshl_add_u64 v[42:43], v[2:3], 0, s[0:1]
	s_mov_b64 s[0:1], 0x2400000
	v_add_u32_e32 v90, 0x140, v89
	v_add_u32_e32 v103, 0x120, v102
	v_add_u32_e32 v104, 0x240, v102
	v_add_u32_e32 v108, 0x50, v106
	v_cndmask_b32_e64 v36, 0, 1.0, vcc
	v_lshl_add_u64 v[44:45], v[2:3], 0, s[0:1]
	s_add_i32 s54, s48, s52
	v_add_u32_e32 v119, v8, v12
	v_add_u32_e32 v120, v9, v12
	v_add_u32_e32 v121, v10, v7
	v_add_u32_e32 v122, v91, v51
	v_add_u32_e32 v123, v4, v50
	v_add_u32_e32 v124, v4, v13
	v_add_u32_e32 v125, v4, v52
	v_add_u32_e32 v126, v11, v12
	s_mov_b32 s46, s62
	v_mov_b32_e32 v239, 0
	global_load_dword v238, v239, s[4:5]
	global_load_dword v238, v239, s[4:5]
	global_load_dword v238, v239, s[4:5]
	global_load_dword v238, v239, s[4:5]
	global_load_dword v238, v239, s[4:5]
	global_load_dword v238, v239, s[4:5]
	global_load_dword v238, v239, s[4:5]
	global_load_dword v238, v239, s[4:5]
	global_load_dword v238, v239, s[4:5]
	global_load_dword v238, v239, s[4:5]
	global_load_dword v238, v239, s[4:5]
	global_load_dword v238, v239, s[4:5]
	s_branch .LBB0_1219

.LBB0_1219:
	s_waitcnt vmcnt(50)
	v_lshlrev_b32_e32 v2, 16, v67
	v_add_f32_e32 v2, v59, v2
	s_waitcnt vmcnt(45)
	v_lshlrev_b32_e32 v3, 16, v72
	v_mul_f32_e32 v2, 0xbfb8aa3b, v2
	v_add_f32_e32 v3, v59, v3
	s_waitcnt vmcnt(40)
	v_lshlrev_b32_e32 v4, 16, v81
	v_exp_f32_e32 v2, v2
	v_mul_f32_e32 v3, 0xbfb8aa3b, v3
	v_add_f32_e32 v4, v59, v4
	v_exp_f32_e32 v3, v3
	v_mul_f32_e32 v4, 0xbfb8aa3b, v4
	v_exp_f32_e32 v4, v4
	v_add_f32_e32 v2, 1.0, v2
	v_rcp_f32_e32 v2, v2
	v_add_f32_e32 v3, 1.0, v3
	v_rcp_f32_e32 v3, v3
	v_add_f32_e32 v4, 1.0, v4
	s_waitcnt vmcnt(35)
	v_lshlrev_b32_e32 v5, 16, v86
	v_rcp_f32_e32 v4, v4
	v_add_f32_e32 v5, v59, v5
	v_mul_f32_e32 v5, 0xbfb8aa3b, v5
	s_mov_b32 s0, 0xbf1b4598
	v_exp_f32_e32 v5, v5
	v_fma_f32 v139, v2, s0, 0
	v_fmamk_f32 v138, v3, 0xbf1b4598, v139
	v_fmamk_f32 v136, v4, 0xbf1b4598, v138
	s_waitcnt vmcnt(30)
	v_lshlrev_b32_e32 v3, 16, v96
	s_waitcnt vmcnt(25)
	v_lshlrev_b32_e32 v4, 16, v113
	v_add_f32_e32 v3, v59, v3
	v_add_f32_e32 v4, v59, v4
	v_add_f32_e32 v2, 1.0, v5
	v_mul_f32_e32 v3, 0xbfb8aa3b, v3
	v_mul_f32_e32 v4, 0xbfb8aa3b, v4
	v_rcp_f32_e32 v2, v2
	v_exp_f32_e32 v3, v3
	v_exp_f32_e32 v4, v4
	s_waitcnt vmcnt(15)
	v_lshlrev_b32_e32 v5, 16, v130
	v_fmamk_f32 v137, v2, 0xbf1b4598, v136
	v_add_f32_e32 v2, 1.0, v3
	v_add_f32_e32 v3, 1.0, v4
	v_lshlrev_b32_e32 v4, 16, v127
	v_add_f32_e32 v4, v59, v4
	v_mul_f32_e32 v4, 0xbfb8aa3b, v4
	v_add_f32_e32 v5, v59, v5
	v_exp_f32_e32 v4, v4
	v_mul_f32_e32 v5, 0xbfb8aa3b, v5
	v_exp_f32_e32 v5, v5
	v_rcp_f32_e32 v2, v2
	v_rcp_f32_e32 v3, v3
	v_add_f32_e32 v4, 1.0, v4
	v_rcp_f32_e32 v4, v4
	v_add_f32_e32 v5, 1.0, v5
	v_rcp_f32_e32 v5, v5
	v_fmamk_f32 v135, v2, 0xbf1b4598, v137
	v_lshlrev_b32_e32 v9, 16, v23
	v_lshlrev_b32_e32 v8, 16, v30
	v_fmamk_f32 v134, v3, 0xbf1b4598, v135
	v_pk_mul_f32 v[6:7], v[18:19], v[8:9] op_sel_hi:[0,1]
	v_fmamk_f32 v133, v4, 0xbf1b4598, v134
	v_pk_mul_f32 v[140:141], v[6:7], v[6:7]
	v_fmamk_f32 v14, v5, 0xbf1b4598, v133
	v_lshlrev_b32_e32 v5, 16, v29
	v_lshlrev_b32_e32 v4, 16, v46
	v_add_f32_dpp v141, v141, v141 quad_perm:[1,0,3,2] row_mask:0xf bank_mask:0xf bound_ctrl:1
	v_pk_mul_f32 v[2:3], v[18:19], v[4:5] op_sel_hi:[0,1]
	v_lshlrev_b32_e32 v55, 16, v1
	v_add_f32_dpp v141, v141, v141 quad_perm:[2,3,0,1] row_mask:0xf bank_mask:0xf bound_ctrl:1
	v_lshlrev_b32_e32 v54, 16, v20
	v_pk_mul_f32 v[142:143], v[2:3], v[2:3]
	v_add_f32_dpp v141, v141, v141 row_ror:4 row_mask:0xf bank_mask:0xf bound_ctrl:1
	v_pk_mul_f32 v[52:53], v[18:19], v[54:55] op_sel_hi:[0,1]
	v_pk_mul_f32 v[10:11], v[52:53], v[52:53]
	v_add_f32_dpp v146, v141, v141 row_ror:8 row_mask:0xf bank_mask:0xf bound_ctrl:1
	v_add_f32_dpp v141, v142, v142 quad_perm:[1,0,3,2] row_mask:0xf bank_mask:0xf bound_ctrl:1
	v_lshlrev_b32_e32 v51, 16, v19
	v_lshlrev_b32_e32 v50, 16, v24
	v_add_f32_dpp v141, v141, v141 quad_perm:[2,3,0,1] row_mask:0xf bank_mask:0xf bound_ctrl:1
	v_pk_mul_f32 v[12:13], v[18:19], v[50:51] op_sel_hi:[0,1]
	v_add_f32_dpp v10, v10, v10 quad_perm:[1,0,3,2] row_mask:0xf bank_mask:0xf bound_ctrl:1
	v_add_f32_dpp v11, v11, v11 quad_perm:[1,0,3,2] row_mask:0xf bank_mask:0xf bound_ctrl:1
	v_add_f32_dpp v141, v141, v141 row_ror:4 row_mask:0xf bank_mask:0xf bound_ctrl:1
	v_pk_mul_f32 v[56:57], v[12:13], v[12:13]
	v_add_f32_dpp v10, v10, v10 quad_perm:[2,3,0,1] row_mask:0xf bank_mask:0xf bound_ctrl:1
	v_add_f32_dpp v11, v11, v11 quad_perm:[2,3,0,1] row_mask:0xf bank_mask:0xf bound_ctrl:1
	v_add_f32_dpp v147, v141, v141 row_ror:8 row_mask:0xf bank_mask:0xf bound_ctrl:1
	v_add_f32_dpp v141, v143, v143 quad_perm:[1,0,3,2] row_mask:0xf bank_mask:0xf bound_ctrl:1
	v_add_f32_dpp v10, v10, v10 row_ror:4 row_mask:0xf bank_mask:0xf bound_ctrl:1
	v_add_f32_dpp v11, v11, v11 row_ror:4 row_mask:0xf bank_mask:0xf bound_ctrl:1
	v_add_f32_dpp v56, v56, v56 quad_perm:[1,0,3,2] row_mask:0xf bank_mask:0xf bound_ctrl:1
	v_add_f32_dpp v57, v57, v57 quad_perm:[1,0,3,2] row_mask:0xf bank_mask:0xf bound_ctrl:1
	v_add_f32_dpp v141, v141, v141 quad_perm:[2,3,0,1] row_mask:0xf bank_mask:0xf bound_ctrl:1
	v_add_f32_dpp v10, v10, v10 row_ror:8 row_mask:0xf bank_mask:0xf bound_ctrl:1
	v_add_f32_dpp v11, v11, v11 row_ror:8 row_mask:0xf bank_mask:0xf bound_ctrl:1
	v_add_f32_dpp v56, v56, v56 quad_perm:[2,3,0,1] row_mask:0xf bank_mask:0xf bound_ctrl:1
	v_add_f32_dpp v57, v57, v57 quad_perm:[2,3,0,1] row_mask:0xf bank_mask:0xf bound_ctrl:1
	v_add_f32_dpp v141, v141, v141 row_ror:4 row_mask:0xf bank_mask:0xf bound_ctrl:1
	v_add_f32_dpp v56, v56, v56 row_ror:4 row_mask:0xf bank_mask:0xf bound_ctrl:1
	v_add_f32_dpp v57, v57, v57 row_ror:4 row_mask:0xf bank_mask:0xf bound_ctrl:1
	v_add_f32_dpp v148, v141, v141 row_ror:8 row_mask:0xf bank_mask:0xf bound_ctrl:1
	ds_bpermute_b32 v141, v98, v10
	ds_bpermute_b32 v142, v98, v11
	v_add_f32_dpp v56, v56, v56 row_ror:8 row_mask:0xf bank_mask:0xf bound_ctrl:1
	v_add_f32_dpp v57, v57, v57 row_ror:8 row_mask:0xf bank_mask:0xf bound_ctrl:1
	ds_bpermute_b32 v143, v98, v56
	ds_bpermute_b32 v144, v98, v57
	s_waitcnt lgkmcnt(0)
	s_barrier
	ds_write_b32 v82, v14 offset:64000
	v_add_f32_dpp v140, v140, v140 quad_perm:[1,0,3,2] row_mask:0xf bank_mask:0xf bound_ctrl:1
	s_waitcnt lgkmcnt(0)
	s_barrier
	s_waitcnt lgkmcnt(4)
	v_add_f32_e32 v141, v10, v141
	v_add_f32_dpp v140, v140, v140 quad_perm:[2,3,0,1] row_mask:0xf bank_mask:0xf bound_ctrl:1
	s_waitcnt lgkmcnt(3)
	v_add_f32_e32 v142, v11, v142
	ds_read2st64_b32 v[10:11], v83 offset0:250 offset1:251
	v_add_f32_dpp v140, v140, v140 row_ror:4 row_mask:0xf bank_mask:0xf bound_ctrl:1
	s_waitcnt lgkmcnt(3)
	v_add_f32_e32 v143, v56, v143
	s_waitcnt lgkmcnt(2)
	v_add_f32_e32 v144, v57, v144
	v_add_f32_dpp v140, v140, v140 row_ror:8 row_mask:0xf bank_mask:0xf bound_ctrl:1
	ds_read2st64_b32 v[56:57], v83 offset0:252 offset1:253
	ds_bpermute_b32 v145, v98, v140
	ds_bpermute_b32 v149, v98, v146
	ds_bpermute_b32 v150, v98, v147
	ds_bpermute_b32 v151, v98, v148
	s_waitcnt lgkmcnt(5)
	v_add_f32_e32 v156, 0, v10
	v_add_f32_e32 v10, v156, v11
	s_waitcnt lgkmcnt(4)
	v_add_f32_e32 v10, v10, v56
	s_waitcnt lgkmcnt(3)
	v_add_f32_e32 v145, v140, v145
	s_waitcnt lgkmcnt(2)
	v_add_f32_e32 v146, v146, v149
	s_waitcnt lgkmcnt(1)
	v_add_f32_e32 v147, v147, v150
	s_waitcnt lgkmcnt(0)
	v_add_f32_e32 v140, v148, v151
	v_add_f32_e32 v10, v10, v57
	ds_bpermute_b32 v149, v99, v141
	ds_bpermute_b32 v150, v99, v142
	ds_bpermute_b32 v151, v99, v143
	ds_bpermute_b32 v152, v99, v144
	ds_bpermute_b32 v153, v99, v145
	ds_bpermute_b32 v154, v99, v146
	ds_bpermute_b32 v155, v99, v147
	ds_bpermute_b32 v148, v99, v140
	v_mul_f32_e32 v10, 0x3fb8aa3b, v10
	v_exp_f32_e32 v10, v10
	s_add_i32 s44, s48, s46
	s_and_saveexec_b64 s[0:1], s[8:9]
	s_cbranch_execz .LBB0_1221
	s_ashr_i32 s45, s44, 31
	s_lshl_b64 s[56:57], s[44:45], 8
	v_lshl_add_u64 v[158:159], v[26:27], 0, s[56:57]
	global_store_dword v[158:159], v10, off
.LBB0_1221:
	s_or_b64 exec, exec, s[0:1]
	v_lshlrev_b32_e32 v57, 16, v68
	v_add_f32_e32 v57, v60, v57
	v_lshlrev_b32_e32 v157, 16, v75
	v_mul_f32_e32 v57, 0xbfb8aa3b, v57
	v_add_f32_e32 v157, v60, v157
	v_exp_f32_e32 v57, v57
	v_mul_f32_e32 v157, 0xbfb8aa3b, v157
	v_exp_f32_e32 v157, v157
	v_lshlrev_b32_e32 v159, 16, v87
	v_add_f32_e32 v57, 1.0, v57
	v_rcp_f32_e32 v158, v57
	v_add_f32_e32 v57, 1.0, v157
	v_lshlrev_b32_e32 v157, 16, v84
	v_add_f32_e32 v157, v60, v157
	v_mul_f32_e32 v157, 0xbfb8aa3b, v157
	v_add_f32_e32 v159, v60, v159
	v_exp_f32_e32 v157, v157
	v_mul_f32_e32 v159, 0xbfb8aa3b, v159
	v_exp_f32_e32 v161, v159
	v_rcp_f32_e32 v159, v57
	v_add_f32_e32 v57, 1.0, v157
	v_lshlrev_b32_e32 v157, 16, v100
	v_rcp_f32_e32 v160, v57
	v_add_f32_e32 v57, 1.0, v161
	v_add_f32_e32 v157, v60, v157
	v_lshlrev_b32_e32 v161, 16, v114
	v_mul_f32_e32 v157, 0xbfb8aa3b, v157
	v_add_f32_e32 v161, v60, v161
	v_exp_f32_e32 v157, v157
	v_mul_f32_e32 v161, 0xbfb8aa3b, v161
	v_exp_f32_e32 v163, v161
	v_rcp_f32_e32 v161, v57
	v_add_f32_e32 v57, 1.0, v157
	v_lshlrev_b32_e32 v157, 16, v128
	v_rcp_f32_e32 v162, v57
	v_add_f32_e32 v57, 1.0, v163
	v_add_f32_e32 v157, v60, v157
	s_waitcnt vmcnt(14)
	v_lshlrev_b32_e32 v163, 16, v131
	v_mul_f32_e32 v157, 0xbfb8aa3b, v157
	v_add_f32_e32 v163, v60, v163
	v_exp_f32_e32 v157, v157
	v_mul_f32_e32 v163, 0xbfb8aa3b, v163
	v_exp_f32_e32 v165, v163
	v_rcp_f32_e32 v163, v57
	v_add_f32_e32 v57, 1.0, v157
	v_rcp_f32_e32 v164, v57
	v_add_f32_e32 v57, 1.0, v165
	v_rcp_f32_e32 v165, v57
	s_waitcnt lgkmcnt(7)
	v_add_f32_e32 v57, v141, v149
	s_waitcnt lgkmcnt(6)
	v_add_f32_e32 v141, v142, v150
	v_cndmask_b32_e64 v142, v156, 0, s[8:9]
	v_cndmask_b32_e64 v11, 0, v11, s[10:11]
	v_add_f32_e32 v11, v142, v11
	v_cndmask_b32_e64 v56, 0, v56, s[12:13]
	v_add_f32_e32 v11, v11, v56
	v_add_f32_e32 v57, 0x2b8cbccc, v57
	s_waitcnt lgkmcnt(5)
	v_add_f32_e32 v150, v143, v151
	s_waitcnt lgkmcnt(4)
	v_add_f32_e32 v151, v144, v152
	v_add_f32_e32 v56, v139, v11
	v_rsq_f32_e32 v144, v57
	v_add_f32_e32 v57, v138, v11
	v_mul_f32_e32 v56, 0x3fb8aa3b, v56
	v_mul_f32_e32 v57, 0x3fb8aa3b, v57
	v_exp_f32_e32 v56, v56
	v_exp_f32_e32 v57, v57
	v_add_f32_e32 v141, 0x2b8cbccc, v141
	s_waitcnt lgkmcnt(3)
	v_add_f32_e32 v152, v145, v153
	v_rsq_f32_e32 v145, v141
	v_mul_f32_e32 v139, 0x3fb8aa3b, v11
	s_waitcnt lgkmcnt(2)
	v_add_f32_e32 v153, v146, v154
	s_waitcnt lgkmcnt(1)
	v_add_f32_e32 v154, v147, v155
	s_waitcnt lgkmcnt(0)
	v_add_f32_e32 v155, v140, v148
	v_exp_f32_e32 v140, v139
	v_rcp_f32_e32 v142, v56
	v_rcp_f32_e32 v143, v57
	v_pk_add_f32 v[138:139], v[158:159], -1.0 op_sel_hi:[1,0]
	v_pk_mul_f32 v[52:53], v[52:53], v[144:145]
	v_pk_fma_f32 v[138:139], v[16:17], v[138:139], 1.0 op_sel_hi:[0,1,0]
	v_pk_mul_f32 v[144:145], v[158:159], v[52:53]
	v_mov_b32_e32 v141, v56
	v_lshlrev_b32_e32 v147, 16, v17
	v_lshlrev_b32_e32 v146, 16, v22
	v_pk_mul_f32 v[54:55], v[138:139], v[54:55]
	v_pk_mul_f32 v[138:139], v[10:11], v[142:143] op_sel_hi:[0,1]
	v_pk_mul_f32 v[52:53], v[140:141], v[52:53] neg_lo:[0,1] neg_hi:[0,1]
	v_pk_mul_f32 v[140:141], v[144:145], v[142:143]
	v_pk_mul_f32 v[146:147], v[56:57], v[146:147]
	v_pk_mul_f32 v[148:149], v[54:55], v[138:139]
	v_pk_mul_f32 v[54:55], v[54:55], v[142:143]
	v_pk_mul_f32 v[138:139], v[144:145], v[138:139]
	v_cvt_pk_bf16_f32 v52, v52, v53
	v_cvt_pk_bf16_f32 v53, v140, v141
	v_cvt_pk_bf16_f32 v54, v54, v55
	v_cvt_pk_bf16_f32 v55, v146, v147
	v_cvt_pk_bf16_f32 v56, v138, v139
	v_cvt_pk_bf16_f32 v138, v148, v149
	ds_write_b16 v101, v52
	ds_write_b16_d16_hi v101, v52 offset:144
	ds_write_b16 v101, v53 offset:4608
	ds_write_b16_d16_hi v101, v53 offset:4752
	ds_write_b16 v101, v54 offset:9216
	ds_write_b16_d16_hi v101, v54 offset:9360
	ds_write_b16 v101, v55 offset:13824
	ds_write_b16_d16_hi v101, v55 offset:13968
	ds_write_b16 v101, v56 offset:18432
	ds_write_b16_d16_hi v101, v56 offset:18576
	ds_write_b16 v101, v138 offset:23040
	v_add_f32_e32 v53, 0x2b8cbccc, v150
	v_add_f32_e32 v52, v136, v11
	v_rsq_f32_e32 v136, v53
	v_add_f32_e32 v53, v137, v11
	v_mul_f32_e32 v52, 0x3fb8aa3b, v52
	v_mul_f32_e32 v53, 0x3fb8aa3b, v53
	v_exp_f32_e32 v52, v52
	v_exp_f32_e32 v53, v53
	v_add_f32_e32 v56, 0x2b8cbccc, v151
	v_rsq_f32_e32 v137, v56
	v_rcp_f32_e32 v54, v52
	v_rcp_f32_e32 v55, v53
	ds_write_b16_d16_hi v101, v138 offset:23184
	ds_write_b16 v101, v69 offset:27648
	ds_write_b16 v101, v80 offset:27792
	v_pk_add_f32 v[138:139], v[160:161], -1.0 op_sel_hi:[1,0]
	v_pk_mul_f32 v[12:13], v[12:13], v[136:137]
	v_pk_fma_f32 v[138:139], v[16:17], v[138:139], 1.0 op_sel_hi:[0,1,0]
	v_pk_mul_f32 v[50:51], v[138:139], v[50:51]
	v_pk_mul_f32 v[138:139], v[10:11], v[54:55] op_sel_hi:[0,1]
	v_pk_mul_f32 v[136:137], v[160:161], v[12:13]
	v_mov_b32_e32 v56, v57
	v_mov_b32_e32 v57, v52
	v_lshlrev_b32_e32 v141, 16, v21
	v_lshlrev_b32_e32 v140, 16, v28
	v_pk_mul_f32 v[142:143], v[50:51], v[138:139]
	v_pk_mul_f32 v[50:51], v[50:51], v[54:55]
	v_pk_mul_f32 v[12:13], v[56:57], v[12:13] neg_lo:[0,1] neg_hi:[0,1]
	v_pk_mul_f32 v[54:55], v[136:137], v[54:55]
	v_pk_mul_f32 v[140:141], v[52:53], v[140:141]
	v_pk_mul_f32 v[56:57], v[136:137], v[138:139]
	v_cvt_pk_bf16_f32 v12, v12, v13
	v_cvt_pk_bf16_f32 v13, v54, v55
	v_cvt_pk_bf16_f32 v50, v50, v51
	v_cvt_pk_bf16_f32 v51, v140, v141
	v_cvt_pk_bf16_f32 v52, v56, v57
	v_cvt_pk_bf16_f32 v54, v142, v143
	ds_write_b16 v102, v12
	ds_write_b16_d16_hi v102, v12 offset:144
	ds_write_b16 v102, v13 offset:4608
	ds_write_b16_d16_hi v102, v13 offset:4752
	ds_write_b16 v102, v50 offset:9216
	ds_write_b16_d16_hi v102, v50 offset:9360
	ds_write_b16 v102, v51 offset:13824
	ds_write_b16_d16_hi v102, v51 offset:13968
	ds_write_b16 v102, v52 offset:18432
	ds_write_b16_d16_hi v102, v52 offset:18576
	ds_write_b16 v102, v54 offset:23040
	v_add_f32_e32 v13, 0x2b8cbccc, v152
	v_add_f32_e32 v12, v135, v11
	ds_write_b16_d16_hi v102, v54 offset:23184
	ds_write_b16 v102, v85 offset:27648
	ds_write_b16 v102, v88 offset:27792
	v_rsq_f32_e32 v54, v13
	v_add_f32_e32 v13, v134, v11
	v_mul_f32_e32 v12, 0x3fb8aa3b, v12
	v_mul_f32_e32 v13, 0x3fb8aa3b, v13
	v_exp_f32_e32 v12, v12
	v_exp_f32_e32 v13, v13
	v_add_f32_e32 v52, 0x2b8cbccc, v153
	v_rsq_f32_e32 v55, v52
	v_rcp_f32_e32 v50, v12
	v_rcp_f32_e32 v51, v13
	v_pk_add_f32 v[56:57], v[162:163], -1.0 op_sel_hi:[1,0]
	v_pk_mul_f32 v[6:7], v[6:7], v[54:55]
	v_pk_fma_f32 v[56:57], v[16:17], v[56:57], 1.0 op_sel_hi:[0,1,0]
	v_pk_mul_f32 v[8:9], v[56:57], v[8:9]
	v_pk_mul_f32 v[56:57], v[10:11], v[50:51] op_sel_hi:[0,1]
	v_pk_mul_f32 v[54:55], v[162:163], v[6:7]
	v_mov_b32_e32 v52, v53
	v_mov_b32_e32 v53, v12
	v_lshlrev_b32_e32 v135, 16, v25
	v_lshlrev_b32_e32 v134, 16, v32
	v_pk_mul_f32 v[136:137], v[8:9], v[56:57]
	v_pk_mul_f32 v[8:9], v[8:9], v[50:51]
	v_pk_mul_f32 v[6:7], v[52:53], v[6:7] neg_lo:[0,1] neg_hi:[0,1]
	v_pk_mul_f32 v[50:51], v[54:55], v[50:51]
	v_pk_mul_f32 v[134:135], v[12:13], v[134:135]
	v_pk_mul_f32 v[52:53], v[54:55], v[56:57]
	v_cvt_pk_bf16_f32 v6, v6, v7
	v_cvt_pk_bf16_f32 v7, v50, v51
	v_cvt_pk_bf16_f32 v8, v8, v9
	v_cvt_pk_bf16_f32 v9, v134, v135
	v_cvt_pk_bf16_f32 v12, v52, v53
	v_cvt_pk_bf16_f32 v50, v136, v137
	ds_write_b16 v103, v6
	ds_write_b16_d16_hi v103, v6 offset:144
	ds_write_b16 v103, v7 offset:4608
	ds_write_b16_d16_hi v103, v7 offset:4752
	ds_write_b16 v103, v8 offset:9216
	ds_write_b16_d16_hi v103, v8 offset:9360
	ds_write_b16 v103, v9 offset:13824
	ds_write_b16_d16_hi v103, v9 offset:13968
	ds_write_b16 v103, v12 offset:18432
	ds_write_b16_d16_hi v103, v12 offset:18576
	ds_write_b16 v103, v50 offset:23040
	v_add_f32_e32 v7, 0x2b8cbccc, v154
	v_add_f32_e32 v6, v133, v11
	ds_write_b16_d16_hi v103, v50 offset:23184
	ds_write_b16 v103, v107 offset:27648
	ds_write_b16 v103, v118 offset:27792
	v_rsq_f32_e32 v50, v7
	v_add_f32_e32 v7, v14, v11
	v_mul_f32_e32 v6, 0x3fb8aa3b, v6
	v_mul_f32_e32 v7, 0x3fb8aa3b, v7
	v_exp_f32_e32 v6, v6
	v_exp_f32_e32 v7, v7
	v_add_f32_e32 v11, 0x2b8cbccc, v155
	v_rsq_f32_e32 v51, v11
	v_rcp_f32_e32 v8, v6
	v_rcp_f32_e32 v9, v7
	v_pk_add_f32 v[52:53], v[164:165], -1.0 op_sel_hi:[1,0]
	s_add_i32 s55, s46, s52
	v_pk_fma_f32 v[52:53], v[16:17], v[52:53], 1.0 op_sel_hi:[0,1,0]
	v_pk_mul_f32 v[2:3], v[2:3], v[50:51]
	v_mov_b32_e32 v12, v13
	v_mov_b32_e32 v13, v6
	s_cmpk_gt_i32 s55, 0x1fff
	s_waitcnt vmcnt(13)
	v_lshlrev_b32_e32 v55, 16, v31
	v_lshlrev_b32_e32 v54, 16, v48
	v_pk_mul_f32 v[4:5], v[52:53], v[4:5]
	v_pk_mul_f32 v[10:11], v[10:11], v[8:9] op_sel_hi:[0,1]
	v_pk_mul_f32 v[50:51], v[164:165], v[2:3]
	v_pk_mul_f32 v[2:3], v[12:13], v[2:3] neg_lo:[0,1] neg_hi:[0,1]
	s_cselect_b64 s[0:1], -1, 0
	v_pk_mul_f32 v[54:55], v[6:7], v[54:55]
	v_pk_mul_f32 v[52:53], v[4:5], v[10:11]
	v_pk_mul_f32 v[4:5], v[4:5], v[8:9]
	v_pk_mul_f32 v[6:7], v[50:51], v[8:9]
	v_pk_mul_f32 v[8:9], v[50:51], v[10:11]
	v_cvt_pk_bf16_f32 v2, v2, v3
	s_and_b64 vcc, exec, s[0:1]
	v_cvt_pk_bf16_f32 v3, v6, v7
	v_cvt_pk_bf16_f32 v4, v4, v5
	v_cvt_pk_bf16_f32 v5, v54, v55
	v_cvt_pk_bf16_f32 v6, v8, v9
	v_cvt_pk_bf16_f32 v7, v52, v53
	ds_write_b16 v104, v2
	ds_write_b16_d16_hi v104, v2 offset:144
	ds_write_b16 v104, v3 offset:4608
	ds_write_b16_d16_hi v104, v3 offset:4752
	ds_write_b16 v104, v4 offset:9216
	ds_write_b16_d16_hi v104, v4 offset:9360
	ds_write_b16 v104, v5 offset:13824
	ds_write_b16_d16_hi v104, v5 offset:13968
	ds_write_b16 v104, v6 offset:18432
	ds_write_b16_d16_hi v104, v6 offset:18576
	ds_write_b16 v104, v7 offset:23040
	ds_write_b16_d16_hi v104, v7 offset:23184
	ds_write_b16 v104, v129 offset:27648
	s_waitcnt vmcnt(12)
	ds_write_b16 v104, v132 offset:27792
	s_cbranch_vccnz .LBB0_1223
	s_add_i32 s2, s54, s46
	s_ashr_i32 s3, s2, 31
	s_lshr_b32 s3, s3, 25
	s_add_i32 s3, s2, s3
	s_ashr_i32 s46, s3, 7
	s_and_b32 s3, s3, 0x7ffff80
	s_sub_i32 s2, s2, s3
	s_lshl_b32 s45, s46, 8
	s_and_b32 s3, s46, 1
	s_and_b32 s45, s45, 0x7ff000
	s_lshl_b32 s2, s2, 5
	s_lshl_b32 s46, s46, 5
	s_add_i32 s45, s45, s2
	s_lshl_b32 s2, s3, 9
	s_and_b32 s46, s46, 0x1c0
	s_or_b32 s2, s2, s46
	v_or_b32_e32 v1, s2, v33
	v_lshlrev_b32_e32 v1, 2, v1
	v_or_b32_e32 v6, s46, v33
	s_cmp_eq_u32 s3, 0
	global_load_dword v59, v1, s[4:5]
	global_load_dword v60, v1, s[6:7]
	v_lshlrev_b32_e32 v1, 2, v6
	s_cselect_b64 vcc, -1, 0
	global_load_dword v16, v1, s[30:31]
	global_load_dword v18, v1, s[28:29]
	v_cndmask_b32_e32 v1, v58, v49, vcc
	v_or_b32_e32 v1, s45, v1
	v_lshl_or_b32 v14, v1, 9, v6
	v_lshlrev_b64 v[2:3], 1, v[14:15]
	v_lshl_add_u64 v[4:5], s[36:37], 0, v[2:3]
	global_load_ushort v20, v[4:5], off
	v_lshl_add_u64 v[4:5], s[40:41], 0, v[2:3]
	v_cndmask_b32_e32 v1, v62, v61, vcc
	global_load_ushort v67, v[4:5], off
	v_lshl_add_u64 v[4:5], s[42:43], 0, v[2:3]
	v_or_b32_e32 v1, s45, v1
	global_load_ushort v68, v[4:5], off
	v_lshl_add_u64 v[4:5], s[34:35], 0, v[2:3]
	v_lshl_add_u64 v[2:3], s[38:39], 0, v[2:3]
	v_lshl_or_b32 v14, v1, 9, v6
	global_load_ushort v22, v[4:5], off
	global_load_ushort v69, v[2:3], off
	v_lshlrev_b64 v[2:3], 1, v[14:15]
	v_lshl_add_u64 v[4:5], s[36:37], 0, v[2:3]
	global_load_ushort v1, v[4:5], off
	v_lshl_add_u64 v[4:5], s[40:41], 0, v[2:3]
	global_load_ushort v72, v[4:5], off
	v_lshl_add_u64 v[4:5], s[42:43], 0, v[2:3]
	global_load_ushort v75, v[4:5], off
	v_lshl_add_u64 v[4:5], s[34:35], 0, v[2:3]
	v_lshl_add_u64 v[2:3], s[38:39], 0, v[2:3]
	global_load_ushort v17, v[4:5], off
	global_load_ushort v80, v[2:3], off
	v_cndmask_b32_e32 v2, v64, v63, vcc
	v_or_b32_e32 v2, s45, v2
	v_lshl_or_b32 v14, v2, 9, v6
	v_lshlrev_b64 v[2:3], 1, v[14:15]
	v_lshl_add_u64 v[4:5], s[36:37], 0, v[2:3]
	global_load_ushort v24, v[4:5], off
	v_lshl_add_u64 v[4:5], s[40:41], 0, v[2:3]
	global_load_ushort v81, v[4:5], off
	v_lshl_add_u64 v[4:5], s[42:43], 0, v[2:3]
	global_load_ushort v84, v[4:5], off
	v_lshl_add_u64 v[4:5], s[34:35], 0, v[2:3]
	v_lshl_add_u64 v[2:3], s[38:39], 0, v[2:3]
	global_load_ushort v28, v[4:5], off
	global_load_ushort v85, v[2:3], off
	v_cndmask_b32_e32 v2, v66, v65, vcc
	v_or_b32_e32 v2, s45, v2
	v_lshl_or_b32 v14, v2, 9, v6
	v_lshlrev_b64 v[2:3], 1, v[14:15]
	v_lshl_add_u64 v[4:5], s[36:37], 0, v[2:3]
	global_load_ushort v19, v[4:5], off
	v_lshl_add_u64 v[4:5], s[40:41], 0, v[2:3]
	global_load_ushort v86, v[4:5], off
	v_lshl_add_u64 v[4:5], s[42:43], 0, v[2:3]
	global_load_ushort v87, v[4:5], off
	v_lshl_add_u64 v[4:5], s[34:35], 0, v[2:3]
	v_lshl_add_u64 v[2:3], s[38:39], 0, v[2:3]
	global_load_ushort v21, v[4:5], off
	global_load_ushort v88, v[2:3], off
	v_cndmask_b32_e32 v2, v71, v70, vcc
	v_or_b32_e32 v2, s45, v2
	v_lshl_or_b32 v14, v2, 9, v6
	v_lshlrev_b64 v[2:3], 1, v[14:15]
	v_lshl_add_u64 v[4:5], s[36:37], 0, v[2:3]
	global_load_ushort v30, v[4:5], off
	v_lshl_add_u64 v[4:5], s[40:41], 0, v[2:3]
	global_load_ushort v96, v[4:5], off
	v_lshl_add_u64 v[4:5], s[42:43], 0, v[2:3]
	global_load_ushort v100, v[4:5], off
	v_lshl_add_u64 v[4:5], s[34:35], 0, v[2:3]
	v_lshl_add_u64 v[2:3], s[38:39], 0, v[2:3]
	global_load_ushort v32, v[4:5], off
	global_load_ushort v107, v[2:3], off
	v_cndmask_b32_e32 v2, v74, v73, vcc
	v_or_b32_e32 v2, s45, v2
	v_lshl_or_b32 v14, v2, 9, v6
	v_lshlrev_b64 v[2:3], 1, v[14:15]
	v_lshl_add_u64 v[4:5], s[36:37], 0, v[2:3]
	global_load_ushort v23, v[4:5], off
	v_lshl_add_u64 v[4:5], s[40:41], 0, v[2:3]
	global_load_ushort v113, v[4:5], off
	v_lshl_add_u64 v[4:5], s[42:43], 0, v[2:3]
	global_load_ushort v114, v[4:5], off
	v_lshl_add_u64 v[4:5], s[34:35], 0, v[2:3]
	v_lshl_add_u64 v[2:3], s[38:39], 0, v[2:3]
	global_load_ushort v25, v[4:5], off
	global_load_ushort v118, v[2:3], off
	v_cndmask_b32_e32 v2, v77, v76, vcc
	v_or_b32_e32 v2, s45, v2
	v_lshl_or_b32 v14, v2, 9, v6
	v_lshlrev_b64 v[2:3], 1, v[14:15]
	v_lshl_add_u64 v[4:5], s[36:37], 0, v[2:3]
	global_load_ushort v46, v[4:5], off
	v_lshl_add_u64 v[4:5], s[40:41], 0, v[2:3]
	global_load_ushort v127, v[4:5], off
	v_lshl_add_u64 v[4:5], s[42:43], 0, v[2:3]
	global_load_ushort v128, v[4:5], off
	v_lshl_add_u64 v[4:5], s[34:35], 0, v[2:3]
	v_lshl_add_u64 v[2:3], s[38:39], 0, v[2:3]
	global_load_ushort v48, v[4:5], off
	global_load_ushort v129, v[2:3], off
	v_cndmask_b32_e32 v2, v79, v78, vcc
	v_or_b32_e32 v2, s45, v2
	v_lshl_or_b32 v14, v2, 9, v6
	v_lshlrev_b64 v[2:3], 1, v[14:15]
	v_lshl_add_u64 v[4:5], s[36:37], 0, v[2:3]
	global_load_ushort v29, v[4:5], off
	v_lshl_add_u64 v[4:5], s[40:41], 0, v[2:3]
	global_load_ushort v130, v[4:5], off
	v_lshl_add_u64 v[4:5], s[42:43], 0, v[2:3]
	global_load_ushort v131, v[4:5], off
	v_lshl_add_u64 v[4:5], s[34:35], 0, v[2:3]
	v_lshl_add_u64 v[2:3], s[38:39], 0, v[2:3]
	global_load_ushort v31, v[4:5], off
	global_load_ushort v132, v[2:3], off

.LBB0_3534:
	s_or_b64 exec, exec, s[4:5]
	v_readlane_b32 s0, v232, 39
	v_readlane_b32 s1, v232, 40
	s_andn2_b64 vcc, exec, s[0:1]
	v_readfirstlane_b32 s1, v2
	s_cbranch_vccnz .LBB0_3546
	s_ashr_i32 s8, s1, 8
	s_mul_i32 s0, s8, 0xfe00
	s_lshl_b32 s4, s27, 10
	s_add_i32 s0, s0, 0
	s_lshl_b32 s2, s27, 9
	s_ashr_i32 s5, s4, 31
	s_lshr_b32 s12, s1, 6
	s_bfe_u32 s9, s1, 0x20006
	s_add_i32 s10, s0, 0xb400
	s_add_i32 s11, s0, 0xdc00
	s_ashr_i32 s3, s2, 31
	s_lshl_b64 s[6:7], s[4:5], 2
	v_readlane_b32 s16, v233, 36
	v_readlane_b32 s17, v233, 37
	s_add_u32 s4, s16, s6
	v_readlane_b32 s20, v233, 40
	v_readlane_b32 s30, v233, 50
	s_addc_u32 s5, s17, s7
	v_readlane_b32 s21, v233, 41
	v_readlane_b32 s31, v233, 51
	s_add_u32 s30, s20, s6
	v_readlane_b32 s26, v233, 46
	s_addc_u32 s31, s21, s7
	s_lshl_b64 s[2:3], s[2:3], 2
	v_readlane_b32 s27, v233, 47
	s_add_u32 s34, s26, s2
	v_readlane_b32 s28, v233, 48
	s_addc_u32 s35, s27, s3
	v_readlane_b32 s29, v233, 49
	s_add_u32 s36, s28, s2
	s_addc_u32 s37, s29, s3
	s_add_u32 s38, s48, 0x2b400000
	s_addc_u32 s39, s49, 0
	s_add_u32 s40, s48, 0x2c400000
	s_addc_u32 s41, s49, 0
	s_add_u32 s42, s48, 0x2d400000
	s_addc_u32 s43, s49, 0
	s_add_u32 s44, s48, 0x30400000
	s_addc_u32 s45, s49, 0
	s_add_u32 s46, s48, 0x31400000
	s_addc_u32 s47, s49, 0
	s_add_i32 s2, s8, s60
	s_ashr_i32 s3, s2, 31
	s_lshr_b32 s3, s3, 25
	s_add_i32 s3, s2, s3
	s_ashr_i32 s6, s3, 7
	s_and_b32 s3, s3, 0x7ffff80
	s_sub_i32 s2, s2, s3
	s_lshl_b32 s7, s6, 8
	s_and_b32 s3, s6, 1
	s_and_b32 s7, s7, 0x7ff000
	s_lshl_b32 s2, s2, 5
	s_lshl_b32 s6, s6, 5
	s_add_i32 s7, s7, s2
	s_lshl_b32 s2, s3, 9
	s_and_b32 s6, s6, 0x1c0
	v_and_b32_e32 v33, 63, v2
	s_or_b32 s2, s2, s6
	v_bfe_u32 v3, v2, 6, 2
	s_bfe_u32 s55, s1, 0x10006
	s_bfe_u32 s54, s12, 0x10001
	s_add_i32 s1, s0, 0x3600
	v_or_b32_e32 v1, s2, v33
	v_lshlrev_b32_e32 v1, 2, v1
	v_or_b32_e32 v41, s6, v33
	v_lshlrev_b32_e32 v49, 3, v3
	s_cmp_eq_u32 s3, 0
	global_load_dword v59, v1, s[4:5]
	global_load_dword v60, v1, s[30:31]
	v_lshlrev_b32_e32 v1, 2, v41
	v_xor_b32_e32 v58, 31, v49
	s_cselect_b64 vcc, -1, 0
	global_load_dword v16, v1, s[36:37]
	global_load_dword v18, v1, s[34:35]
	v_cndmask_b32_e32 v1, v58, v49, vcc
	v_or_b32_e32 v1, s7, v1
	v_or_b32_e32 v61, 1, v49
	v_xor_b32_e32 v62, 30, v49
	v_lshl_or_b32 v14, v1, 9, v41
	v_cndmask_b32_e32 v1, v62, v61, vcc
	v_mov_b32_e32 v15, 0
	v_or_b32_e32 v1, s7, v1
	v_lshlrev_b64 v[4:5], 1, v[14:15]
	v_lshl_or_b32 v14, v1, 9, v41
	v_lshl_add_u64 v[6:7], s[40:41], 0, v[4:5]
	v_lshl_add_u64 v[8:9], s[44:45], 0, v[4:5]
	v_lshlrev_b64 v[24:25], 1, v[14:15]
	v_or_b32_e32 v63, 2, v49
	v_xor_b32_e32 v64, 29, v49
	v_lshl_add_u64 v[10:11], s[46:47], 0, v[4:5]
	v_lshl_add_u64 v[12:13], s[38:39], 0, v[4:5]
	v_lshl_add_u64 v[4:5], s[42:43], 0, v[4:5]
	v_lshl_add_u64 v[26:27], s[40:41], 0, v[24:25]
	v_lshl_add_u64 v[28:29], s[44:45], 0, v[24:25]
	v_lshl_add_u64 v[30:31], s[46:47], 0, v[24:25]
	global_load_ushort v20, v[6:7], off
	global_load_ushort v67, v[8:9], off
	global_load_ushort v68, v[10:11], off
	global_load_ushort v22, v[12:13], off
	global_load_ushort v69, v[4:5], off
	global_load_ushort v1, v[26:27], off
	global_load_ushort v72, v[28:29], off
	global_load_ushort v75, v[30:31], off
	v_cndmask_b32_e32 v8, v64, v63, vcc
	v_or_b32_e32 v8, s7, v8
	v_lshl_or_b32 v14, v8, 9, v41
	v_or_b32_e32 v65, 3, v49
	v_xor_b32_e32 v66, 28, v49
	v_lshlrev_b64 v[8:9], 1, v[14:15]
	v_cndmask_b32_e32 v14, v66, v65, vcc
	v_or_b32_e32 v14, s7, v14
	v_lshl_or_b32 v14, v14, 9, v41
	v_lshl_add_u64 v[4:5], s[38:39], 0, v[24:25]
	v_lshl_add_u64 v[12:13], s[44:45], 0, v[8:9]
	v_lshl_add_u64 v[28:29], s[38:39], 0, v[8:9]
	v_lshlrev_b64 v[30:31], 1, v[14:15]
	v_or_b32_e32 v70, 4, v49
	v_xor_b32_e32 v71, 27, v49
	v_lshl_add_u64 v[6:7], s[42:43], 0, v[24:25]
	v_lshl_add_u64 v[10:11], s[40:41], 0, v[8:9]
	v_lshl_add_u64 v[26:27], s[46:47], 0, v[8:9]
	v_lshl_add_u64 v[8:9], s[42:43], 0, v[8:9]
	v_lshl_add_u64 v[34:35], s[40:41], 0, v[30:31]
	global_load_ushort v17, v[4:5], off
	global_load_ushort v80, v[6:7], off
	global_load_ushort v24, v[10:11], off
	global_load_ushort v81, v[12:13], off
	global_load_ushort v84, v[26:27], off
	s_nop 0
	global_load_ushort v28, v[28:29], off
	s_nop 0
	global_load_ushort v85, v[8:9], off
	global_load_ushort v19, v[34:35], off
	v_cndmask_b32_e32 v12, v71, v70, vcc
	v_or_b32_e32 v12, s7, v12
	v_lshl_or_b32 v14, v12, 9, v41
	v_lshl_add_u64 v[4:5], s[44:45], 0, v[30:31]
	v_lshl_add_u64 v[6:7], s[46:47], 0, v[30:31]
	v_lshlrev_b64 v[12:13], 1, v[14:15]
	v_or_b32_e32 v73, 5, v49
	v_xor_b32_e32 v74, 26, v49
	v_lshl_add_u64 v[8:9], s[38:39], 0, v[30:31]
	v_lshl_add_u64 v[10:11], s[42:43], 0, v[30:31]
	v_lshl_add_u64 v[26:27], s[40:41], 0, v[12:13]
	v_lshl_add_u64 v[34:35], s[44:45], 0, v[12:13]
	v_lshl_add_u64 v[36:37], s[46:47], 0, v[12:13]
	v_lshl_add_u64 v[38:39], s[38:39], 0, v[12:13]
	global_load_ushort v86, v[4:5], off
	global_load_ushort v87, v[6:7], off
	global_load_ushort v21, v[8:9], off
	global_load_ushort v88, v[10:11], off
	global_load_ushort v30, v[26:27], off
	global_load_ushort v96, v[34:35], off
	global_load_ushort v100, v[36:37], off
	global_load_ushort v32, v[38:39], off
	v_cndmask_b32_e32 v6, v74, v73, vcc
	v_or_b32_e32 v6, s7, v6
	v_lshl_or_b32 v14, v6, 9, v41
	v_or_b32_e32 v76, 6, v49
	v_xor_b32_e32 v77, 25, v49
	v_lshlrev_b64 v[6:7], 1, v[14:15]
	v_cndmask_b32_e32 v14, v77, v76, vcc
	v_or_b32_e32 v14, s7, v14
	v_lshl_or_b32 v14, v14, 9, v41
	v_lshl_add_u64 v[4:5], s[42:43], 0, v[12:13]
	v_lshl_add_u64 v[10:11], s[44:45], 0, v[6:7]
	v_lshlrev_b64 v[34:35], 1, v[14:15]
	v_or_b32_e32 v78, 7, v49
	v_xor_b32_e32 v79, 24, v49
	v_lshl_add_u64 v[8:9], s[40:41], 0, v[6:7]
	v_lshl_add_u64 v[12:13], s[46:47], 0, v[6:7]
	v_lshl_add_u64 v[26:27], s[38:39], 0, v[6:7]
	v_lshl_add_u64 v[6:7], s[42:43], 0, v[6:7]
	v_lshl_add_u64 v[36:37], s[40:41], 0, v[34:35]
	v_lshl_add_u64 v[38:39], s[44:45], 0, v[34:35]
	global_load_ushort v107, v[4:5], off
	global_load_ushort v23, v[8:9], off
	global_load_ushort v113, v[10:11], off
	global_load_ushort v114, v[12:13], off
	global_load_ushort v25, v[26:27], off
	global_load_ushort v118, v[6:7], off
	global_load_ushort v46, v[36:37], off
	global_load_ushort v127, v[38:39], off
	v_cndmask_b32_e32 v10, v79, v78, vcc
	v_or_b32_e32 v10, s7, v10
	v_lshl_or_b32 v14, v10, 9, v41
	v_lshl_add_u64 v[4:5], s[46:47], 0, v[34:35]
	v_lshlrev_b64 v[10:11], 1, v[14:15]
	v_lshl_add_u64 v[6:7], s[38:39], 0, v[34:35]
	v_lshl_add_u64 v[8:9], s[42:43], 0, v[34:35]
	v_lshl_add_u64 v[12:13], s[40:41], 0, v[10:11]
	v_lshl_add_u64 v[26:27], s[44:45], 0, v[10:11]
	v_lshl_add_u64 v[34:35], s[46:47], 0, v[10:11]
	v_lshl_add_u64 v[36:37], s[38:39], 0, v[10:11]
	v_lshl_add_u64 v[10:11], s[42:43], 0, v[10:11]
	global_load_ushort v128, v[4:5], off
	global_load_ushort v48, v[6:7], off
	global_load_ushort v129, v[8:9], off
	global_load_ushort v29, v[12:13], off
	global_load_ushort v130, v[26:27], off
	global_load_ushort v131, v[34:35], off
	global_load_ushort v31, v[36:37], off
	global_load_ushort v132, v[10:11], off
	v_and_b32_e32 v4, 0xff, v2
	v_lshlrev_b32_e32 v14, 2, v33
	v_bfe_u32 v40, v2, 4, 2
	v_lshl_add_u32 v82, v4, 2, s0
	v_lshl_add_u64 v[4:5], s[48:49], 0, v[14:15]
	s_mov_b64 s[2:3], 0x3ea00000
	v_and_b32_e32 v47, 15, v2
	v_lshl_add_u64 v[26:27], v[4:5], 0, s[2:3]
	v_lshlrev_b32_e32 v4, 2, v40
	s_lshl_b32 s52, s76, 1
	v_cmp_le_u32_e32 vcc, v47, v4
	s_cmp_gt_u32 s9, 1
	v_lshlrev_b32_e32 v11, 3, v40
	v_cndmask_b32_e64 v5, 0, 1, vcc
	v_cmp_lt_u32_e32 vcc, v47, v4
	v_bfe_u32 v12, v2, 2, 2
	v_or_b32_e32 v12, v11, v12
	v_cndmask_b32_e64 v7, 0, 1, vcc
	s_cselect_b64 vcc, -1, 0
	s_and_b64 s[2:3], vcc, exec
	s_cselect_b32 s1, s1, s0
	s_cmp_eq_u32 s55, 0
	s_movk_i32 s2, 0x1200
	s_cselect_b32 s2, s2, 0x2400
	s_add_i32 s2, s0, s2
	v_cndmask_b32_e32 v5, v7, v5, vcc
	s_cmp_eq_u32 s9, 2
	s_mov_b32 s3, 0xe600
	v_and_b32_e32 v7, 48, v2
	v_lshlrev_b32_e32 v2, 3, v2
	s_cselect_b32 s3, s3, 0xf000
	v_add_u32_e32 v8, s1, v7
	v_mul_u32_u24_e32 v13, 40, v12
	s_lshl_b32 s1, s55, 5
	v_and_b32_e32 v2, 24, v2
	v_mul_u32_u24_e32 v12, 0x90, v12
	v_lshl_add_u32 v6, v47, 1, s0
	s_add_i32 s53, s0, s3
	v_lshlrev_b32_e32 v13, 1, v13
	s_add_i32 s3, s1, s0
	v_add3_u32 v92, s0, v12, v2
	v_add3_u32 v89, v13, s3, v2
	v_add_u32_e32 v13, s1, v6
	v_add_u32_e32 v93, 0x240, v92
	s_lshl_b32 s1, s9, 5
	v_add_u32_e32 v9, s2, v7
	s_lshl_b32 s2, s54, 4
	v_add_u32_e32 v94, s1, v92
	v_add_u32_e32 v95, s1, v93
	s_lshl_b32 s12, s55, 3
	s_add_i32 s1, s0, s1
	v_and_b32_e32 v5, 1, v5
	v_cmp_eq_u32_e64 s[6:7], 0, v3
	s_add_u32 s50, s48, s12
	v_cmp_lt_u32_e64 s[12:13], 1, v3
	v_cmp_eq_u32_e64 s[14:15], 3, v3
	v_mul_u32_u24_e32 v3, 0x240, v3
	v_cmp_eq_u32_e64 s[16:17], 1, v5
	v_cndmask_b32_e64 v5, 0, 1, vcc
	v_readlane_b32 s18, v233, 38
	v_readlane_b32 s19, v233, 39
	v_or_b32_e32 v10, s2, v47
	v_add_u32_e32 v11, s1, v11
	v_or_b32_e32 v3, v3, v33
	s_movk_i32 s1, 0x48
	v_or_b32_e32 v5, v4, v5
	v_mul_u32_u24_e32 v10, 40, v10
	v_lshl_or_b32 v36, s55, 4, v47
	v_lshl_add_u32 v101, v3, 1, s0
	v_mad_u32_u24 v3, v63, s1, v33
	v_cmp_gt_u32_e64 s[18:19], v47, v5
	v_or_b32_e32 v5, 2, v4
	v_add_u32_e32 v83, s0, v14
	v_lshl_add_u32 v10, v10, 1, s0
	v_lshl_add_u32 v91, v36, 1, s0
	v_add_u32_e32 v2, s0, v7
	v_lshl_add_u32 v102, v3, 1, s0
	v_cmp_le_u32_e64 s[0:1], v47, v5
	v_xor_b32_e32 v98, 64, v14
	v_xor_b32_e32 v99, 0x80, v14
	v_cndmask_b32_e64 v14, 0, 1, s[0:1]
	v_cmp_lt_u32_e64 s[0:1], v47, v5
	v_readlane_b32 s22, v233, 42
	v_readlane_b32 s23, v233, 43
	v_cndmask_b32_e64 v5, 0, 1, s[0:1]
	v_cndmask_b32_e32 v5, v5, v14, vcc
	v_and_b32_e32 v5, 1, v5
	v_cmp_eq_u32_e64 s[20:21], 1, v5
	v_or_b32_e32 v5, 3, v4
	v_cmp_le_u32_e64 s[0:1], v47, v5
	v_or_b32_e32 v3, 16, v47
	v_readlane_b32 s24, v233, 44
	v_cndmask_b32_e64 v14, 0, 1, s[0:1]
	v_cmp_lt_u32_e64 s[0:1], v47, v5
	v_readlane_b32 s25, v233, 45
	v_or_b32_e32 v34, 19, v4
	v_cndmask_b32_e64 v5, 0, 1, s[0:1]
	v_cndmask_b32_e32 v5, v5, v14, vcc
	v_and_b32_e32 v5, 1, v5
	v_cmp_eq_u32_e64 s[22:23], 1, v5
	v_or_b32_e32 v5, 17, v4
	v_cmp_le_u32_e64 s[0:1], v3, v5
	v_or_b32_e32 v14, 18, v4
	v_or_b32_e32 v4, s2, v4
	v_cndmask_b32_e64 v35, 0, 1, s[0:1]
	v_cmp_lt_u32_e64 s[0:1], v3, v5
	s_movk_i32 s3, 0x90
	v_mul_u32_u24_e32 v50, 0x90, v4
	v_cndmask_b32_e64 v5, 0, 1, s[0:1]
	v_cndmask_b32_e32 v5, v5, v35, vcc
	v_and_b32_e32 v5, 1, v5
	v_cmp_le_u32_e64 s[0:1], v3, v14
	v_cmp_eq_u32_e64 s[24:25], 1, v5
	v_mul_u32_u24_e32 v51, 0x50, v4
	v_cndmask_b32_e64 v5, 0, 1, s[0:1]
	v_cmp_lt_u32_e64 s[0:1], v3, v14
	s_addc_u32 s51, s49, 0
	v_mul_u32_u24_e32 v12, 40, v47
	v_cndmask_b32_e64 v14, 0, 1, s[0:1]
	v_cndmask_b32_e32 v5, v14, v5, vcc
	v_and_b32_e32 v5, 1, v5
	v_cmp_le_u32_e64 s[0:1], v3, v34
	v_cmp_eq_u32_e64 s[26:27], 1, v5
	v_lshl_add_u32 v97, v12, 1, v2
	v_cndmask_b32_e64 v5, 0, 1, s[0:1]
	v_cmp_lt_u32_e64 s[0:1], v3, v34
	v_mul_u32_u24_e32 v3, 40, v3
	v_lshl_add_u32 v117, v3, 1, v2
	v_cndmask_b32_e64 v14, 0, 1, s[0:1]
	v_cndmask_b32_e32 v5, v14, v5, vcc
	v_and_b32_e32 v5, 1, v5
	v_cmp_eq_u32_e64 s[28:29], 1, v5
	v_mul_u32_u24_e32 v5, 40, v4
	v_lshl_add_u32 v106, v5, 1, v13
	v_or_b32_e32 v5, 1, v4
	v_cmp_eq_u32_e32 vcc, v4, v36
	s_movk_i32 s0, 0x50
	v_mul_u32_u24_e32 v105, 0x140, v40
	v_cndmask_b32_e64 v34, 0, 1.0, vcc
	v_cmp_eq_u32_e32 vcc, v5, v36
	v_or_b32_e32 v5, 3, v4
	v_or_b32_e32 v4, 2, v4
	v_cndmask_b32_e64 v35, 0, 1.0, vcc
	v_mul_lo_u32 v111, v5, s0
	v_mul_lo_u32 v52, v5, s3
	v_cmp_eq_u32_e32 vcc, v5, v36
	v_lshlrev_b32_e32 v5, 3, v33
	v_mul_lo_u32 v109, v4, s0
	s_lshl_b32 s0, s55, 6
	v_lshl_or_b32 v14, s9, 11, v5
	v_add_u32_e32 v110, v13, v109
	v_add_u32_e32 v112, v13, v111
	v_mul_lo_u32 v13, v4, s3
	v_cndmask_b32_e64 v37, 0, 1.0, vcc
	v_cmp_eq_u32_e32 vcc, v4, v36
	v_add_u32_e32 v115, s0, v92
	v_add_u32_e32 v116, s0, v93
	v_add_u32_e32 v4, s0, v6
	v_lshl_add_u64 v[2:3], s[48:49], 0, v[14:15]
	s_mov_b64 s[0:1], 0x8400000
	v_lshl_or_b32 v14, s9, 9, v5
	v_lshl_add_u64 v[38:39], v[2:3], 0, s[0:1]
	v_lshl_add_u64 v[2:3], s[48:49], 0, v[14:15]
	s_mov_b64 s[0:1], 0xc400000
	v_lshl_add_u64 v[40:41], v[2:3], 0, s[0:1]
	v_lshlrev_b32_e32 v2, 4, v33
	v_lshl_or_b32 v14, s54, 10, v2
	v_lshl_add_u64 v[2:3], s[50:51], 0, v[14:15]
	s_mov_b64 s[0:1], 0x4400000
	v_mul_u32_u24_e32 v12, 0x90, v47
	v_lshl_add_u64 v[42:43], v[2:3], 0, s[0:1]
	s_mov_b64 s[0:1], 0x2400000
	v_add_u32_e32 v90, 0x140, v89
	v_add_u32_e32 v103, 0x120, v102
	v_add_u32_e32 v104, 0x240, v102
	v_add_u32_e32 v108, 0x50, v106
	v_cndmask_b32_e64 v36, 0, 1.0, vcc
	v_lshl_add_u64 v[44:45], v[2:3], 0, s[0:1]
	s_add_i32 s54, s8, s52
	v_add_u32_e32 v119, v8, v12
	v_add_u32_e32 v120, v9, v12
	v_add_u32_e32 v121, v10, v7
	v_add_u32_e32 v122, v91, v51
	v_add_u32_e32 v123, v4, v50
	v_add_u32_e32 v124, v4, v13
	v_add_u32_e32 v125, v4, v52
	v_add_u32_e32 v126, v11, v12
	s_mov_b32 s50, s60
	v_mov_b32_e32 v239, 0
	global_load_dword v238, v239, s[4:5]
	global_load_dword v238, v239, s[4:5]
	global_load_dword v238, v239, s[4:5]
	global_load_dword v238, v239, s[4:5]
	global_load_dword v238, v239, s[4:5]
	global_load_dword v238, v239, s[4:5]
	global_load_dword v238, v239, s[4:5]
	global_load_dword v238, v239, s[4:5]
	global_load_dword v238, v239, s[4:5]
	global_load_dword v238, v239, s[4:5]
	global_load_dword v238, v239, s[4:5]
	global_load_dword v238, v239, s[4:5]
	s_branch .LBB0_3537

.LBB0_3537:
	s_waitcnt vmcnt(50)
	v_lshlrev_b32_e32 v2, 16, v67
	v_add_f32_e32 v2, v59, v2
	s_waitcnt vmcnt(45)
	v_lshlrev_b32_e32 v3, 16, v72
	v_mul_f32_e32 v2, 0xbfb8aa3b, v2
	v_add_f32_e32 v3, v59, v3
	s_waitcnt vmcnt(40)
	v_lshlrev_b32_e32 v4, 16, v81
	v_exp_f32_e32 v2, v2
	v_mul_f32_e32 v3, 0xbfb8aa3b, v3
	v_add_f32_e32 v4, v59, v4
	v_exp_f32_e32 v3, v3
	v_mul_f32_e32 v4, 0xbfb8aa3b, v4
	v_exp_f32_e32 v4, v4
	v_add_f32_e32 v2, 1.0, v2
	v_rcp_f32_e32 v2, v2
	v_add_f32_e32 v3, 1.0, v3
	v_rcp_f32_e32 v3, v3
	v_add_f32_e32 v4, 1.0, v4
	s_waitcnt vmcnt(35)
	v_lshlrev_b32_e32 v5, 16, v86
	v_rcp_f32_e32 v4, v4
	v_add_f32_e32 v5, v59, v5
	v_mul_f32_e32 v5, 0xbfb8aa3b, v5
	s_mov_b32 s0, 0xbf1b4598
	v_exp_f32_e32 v5, v5
	v_fma_f32 v139, v2, s0, 0
	v_fmamk_f32 v138, v3, 0xbf1b4598, v139
	v_fmamk_f32 v136, v4, 0xbf1b4598, v138
	s_waitcnt vmcnt(30)
	v_lshlrev_b32_e32 v3, 16, v96
	s_waitcnt vmcnt(25)
	v_lshlrev_b32_e32 v4, 16, v113
	v_add_f32_e32 v3, v59, v3
	v_add_f32_e32 v4, v59, v4
	v_add_f32_e32 v2, 1.0, v5
	v_mul_f32_e32 v3, 0xbfb8aa3b, v3
	v_mul_f32_e32 v4, 0xbfb8aa3b, v4
	v_rcp_f32_e32 v2, v2
	v_exp_f32_e32 v3, v3
	v_exp_f32_e32 v4, v4
	s_waitcnt vmcnt(15)
	v_lshlrev_b32_e32 v5, 16, v130
	v_fmamk_f32 v137, v2, 0xbf1b4598, v136
	v_add_f32_e32 v2, 1.0, v3
	v_add_f32_e32 v3, 1.0, v4
	v_lshlrev_b32_e32 v4, 16, v127
	v_add_f32_e32 v4, v59, v4
	v_mul_f32_e32 v4, 0xbfb8aa3b, v4
	v_add_f32_e32 v5, v59, v5
	v_exp_f32_e32 v4, v4
	v_mul_f32_e32 v5, 0xbfb8aa3b, v5
	v_exp_f32_e32 v5, v5
	v_rcp_f32_e32 v2, v2
	v_rcp_f32_e32 v3, v3
	v_add_f32_e32 v4, 1.0, v4
	v_rcp_f32_e32 v4, v4
	v_add_f32_e32 v5, 1.0, v5
	v_rcp_f32_e32 v5, v5
	v_fmamk_f32 v135, v2, 0xbf1b4598, v137
	v_lshlrev_b32_e32 v9, 16, v23
	v_lshlrev_b32_e32 v8, 16, v30
	v_fmamk_f32 v134, v3, 0xbf1b4598, v135
	v_pk_mul_f32 v[6:7], v[18:19], v[8:9] op_sel_hi:[0,1]
	v_fmamk_f32 v133, v4, 0xbf1b4598, v134
	v_pk_mul_f32 v[140:141], v[6:7], v[6:7]
	v_fmamk_f32 v14, v5, 0xbf1b4598, v133
	v_lshlrev_b32_e32 v5, 16, v29
	v_lshlrev_b32_e32 v4, 16, v46
	v_add_f32_dpp v141, v141, v141 quad_perm:[1,0,3,2] row_mask:0xf bank_mask:0xf bound_ctrl:1
	v_pk_mul_f32 v[2:3], v[18:19], v[4:5] op_sel_hi:[0,1]
	v_lshlrev_b32_e32 v55, 16, v1
	v_add_f32_dpp v141, v141, v141 quad_perm:[2,3,0,1] row_mask:0xf bank_mask:0xf bound_ctrl:1
	v_lshlrev_b32_e32 v54, 16, v20
	v_pk_mul_f32 v[142:143], v[2:3], v[2:3]
	v_add_f32_dpp v141, v141, v141 row_ror:4 row_mask:0xf bank_mask:0xf bound_ctrl:1
	v_pk_mul_f32 v[52:53], v[18:19], v[54:55] op_sel_hi:[0,1]
	v_pk_mul_f32 v[10:11], v[52:53], v[52:53]
	v_add_f32_dpp v146, v141, v141 row_ror:8 row_mask:0xf bank_mask:0xf bound_ctrl:1
	v_add_f32_dpp v141, v142, v142 quad_perm:[1,0,3,2] row_mask:0xf bank_mask:0xf bound_ctrl:1
	v_lshlrev_b32_e32 v51, 16, v19
	v_lshlrev_b32_e32 v50, 16, v24
	v_add_f32_dpp v141, v141, v141 quad_perm:[2,3,0,1] row_mask:0xf bank_mask:0xf bound_ctrl:1
	v_pk_mul_f32 v[12:13], v[18:19], v[50:51] op_sel_hi:[0,1]
	v_add_f32_dpp v10, v10, v10 quad_perm:[1,0,3,2] row_mask:0xf bank_mask:0xf bound_ctrl:1
	v_add_f32_dpp v11, v11, v11 quad_perm:[1,0,3,2] row_mask:0xf bank_mask:0xf bound_ctrl:1
	v_add_f32_dpp v141, v141, v141 row_ror:4 row_mask:0xf bank_mask:0xf bound_ctrl:1
	v_pk_mul_f32 v[56:57], v[12:13], v[12:13]
	v_add_f32_dpp v10, v10, v10 quad_perm:[2,3,0,1] row_mask:0xf bank_mask:0xf bound_ctrl:1
	v_add_f32_dpp v11, v11, v11 quad_perm:[2,3,0,1] row_mask:0xf bank_mask:0xf bound_ctrl:1
	v_add_f32_dpp v147, v141, v141 row_ror:8 row_mask:0xf bank_mask:0xf bound_ctrl:1
	v_add_f32_dpp v141, v143, v143 quad_perm:[1,0,3,2] row_mask:0xf bank_mask:0xf bound_ctrl:1
	v_add_f32_dpp v10, v10, v10 row_ror:4 row_mask:0xf bank_mask:0xf bound_ctrl:1
	v_add_f32_dpp v11, v11, v11 row_ror:4 row_mask:0xf bank_mask:0xf bound_ctrl:1
	v_add_f32_dpp v56, v56, v56 quad_perm:[1,0,3,2] row_mask:0xf bank_mask:0xf bound_ctrl:1
	v_add_f32_dpp v57, v57, v57 quad_perm:[1,0,3,2] row_mask:0xf bank_mask:0xf bound_ctrl:1
	v_add_f32_dpp v141, v141, v141 quad_perm:[2,3,0,1] row_mask:0xf bank_mask:0xf bound_ctrl:1
	v_add_f32_dpp v10, v10, v10 row_ror:8 row_mask:0xf bank_mask:0xf bound_ctrl:1
	v_add_f32_dpp v11, v11, v11 row_ror:8 row_mask:0xf bank_mask:0xf bound_ctrl:1
	v_add_f32_dpp v56, v56, v56 quad_perm:[2,3,0,1] row_mask:0xf bank_mask:0xf bound_ctrl:1
	v_add_f32_dpp v57, v57, v57 quad_perm:[2,3,0,1] row_mask:0xf bank_mask:0xf bound_ctrl:1
	v_add_f32_dpp v141, v141, v141 row_ror:4 row_mask:0xf bank_mask:0xf bound_ctrl:1
	v_add_f32_dpp v56, v56, v56 row_ror:4 row_mask:0xf bank_mask:0xf bound_ctrl:1
	v_add_f32_dpp v57, v57, v57 row_ror:4 row_mask:0xf bank_mask:0xf bound_ctrl:1
	v_add_f32_dpp v148, v141, v141 row_ror:8 row_mask:0xf bank_mask:0xf bound_ctrl:1
	ds_bpermute_b32 v141, v98, v10
	ds_bpermute_b32 v142, v98, v11
	v_add_f32_dpp v56, v56, v56 row_ror:8 row_mask:0xf bank_mask:0xf bound_ctrl:1
	v_add_f32_dpp v57, v57, v57 row_ror:8 row_mask:0xf bank_mask:0xf bound_ctrl:1
	ds_bpermute_b32 v143, v98, v56
	ds_bpermute_b32 v144, v98, v57
	s_waitcnt lgkmcnt(0)
	s_barrier
	ds_write_b32 v82, v14 offset:64000
	v_add_f32_dpp v140, v140, v140 quad_perm:[1,0,3,2] row_mask:0xf bank_mask:0xf bound_ctrl:1
	s_waitcnt lgkmcnt(0)
	s_barrier
	s_waitcnt lgkmcnt(4)
	v_add_f32_e32 v141, v10, v141
	v_add_f32_dpp v140, v140, v140 quad_perm:[2,3,0,1] row_mask:0xf bank_mask:0xf bound_ctrl:1
	s_waitcnt lgkmcnt(3)
	v_add_f32_e32 v142, v11, v142
	ds_read2st64_b32 v[10:11], v83 offset0:250 offset1:251
	v_add_f32_dpp v140, v140, v140 row_ror:4 row_mask:0xf bank_mask:0xf bound_ctrl:1
	s_waitcnt lgkmcnt(3)
	v_add_f32_e32 v143, v56, v143
	s_waitcnt lgkmcnt(2)
	v_add_f32_e32 v144, v57, v144
	v_add_f32_dpp v140, v140, v140 row_ror:8 row_mask:0xf bank_mask:0xf bound_ctrl:1
	ds_read2st64_b32 v[56:57], v83 offset0:252 offset1:253
	ds_bpermute_b32 v145, v98, v140
	ds_bpermute_b32 v149, v98, v146
	ds_bpermute_b32 v150, v98, v147
	ds_bpermute_b32 v151, v98, v148
	s_waitcnt lgkmcnt(5)
	v_add_f32_e32 v156, 0, v10
	v_add_f32_e32 v10, v156, v11
	s_waitcnt lgkmcnt(4)
	v_add_f32_e32 v10, v10, v56
	s_waitcnt lgkmcnt(3)
	v_add_f32_e32 v145, v140, v145
	s_waitcnt lgkmcnt(2)
	v_add_f32_e32 v146, v146, v149
	s_waitcnt lgkmcnt(1)
	v_add_f32_e32 v147, v147, v150
	s_waitcnt lgkmcnt(0)
	v_add_f32_e32 v140, v148, v151
	v_add_f32_e32 v10, v10, v57
	ds_bpermute_b32 v149, v99, v141
	ds_bpermute_b32 v150, v99, v142
	ds_bpermute_b32 v151, v99, v143
	ds_bpermute_b32 v152, v99, v144
	ds_bpermute_b32 v153, v99, v145
	ds_bpermute_b32 v154, v99, v146
	ds_bpermute_b32 v155, v99, v147
	ds_bpermute_b32 v148, v99, v140
	v_mul_f32_e32 v10, 0x3fb8aa3b, v10
	v_exp_f32_e32 v10, v10
	s_add_i32 s48, s8, s50
	s_and_saveexec_b64 s[0:1], s[6:7]
	s_cbranch_execz .LBB0_3539
	s_ashr_i32 s49, s48, 31
	s_lshl_b64 s[2:3], s[48:49], 8
	v_lshl_add_u64 v[158:159], v[26:27], 0, s[2:3]
	global_store_dword v[158:159], v10, off
.LBB0_3539:
	s_or_b64 exec, exec, s[0:1]
	v_lshlrev_b32_e32 v57, 16, v68
	v_add_f32_e32 v57, v60, v57
	v_lshlrev_b32_e32 v157, 16, v75
	v_mul_f32_e32 v57, 0xbfb8aa3b, v57
	v_add_f32_e32 v157, v60, v157
	v_exp_f32_e32 v57, v57
	v_mul_f32_e32 v157, 0xbfb8aa3b, v157
	v_exp_f32_e32 v157, v157
	v_lshlrev_b32_e32 v159, 16, v87
	v_add_f32_e32 v57, 1.0, v57
	v_rcp_f32_e32 v158, v57
	v_add_f32_e32 v57, 1.0, v157
	v_lshlrev_b32_e32 v157, 16, v84
	v_add_f32_e32 v157, v60, v157
	v_mul_f32_e32 v157, 0xbfb8aa3b, v157
	v_add_f32_e32 v159, v60, v159
	v_exp_f32_e32 v157, v157
	v_mul_f32_e32 v159, 0xbfb8aa3b, v159
	v_exp_f32_e32 v161, v159
	v_rcp_f32_e32 v159, v57
	v_add_f32_e32 v57, 1.0, v157
	v_lshlrev_b32_e32 v157, 16, v100
	v_rcp_f32_e32 v160, v57
	v_add_f32_e32 v57, 1.0, v161
	v_add_f32_e32 v157, v60, v157
	v_lshlrev_b32_e32 v161, 16, v114
	v_mul_f32_e32 v157, 0xbfb8aa3b, v157
	v_add_f32_e32 v161, v60, v161
	v_exp_f32_e32 v157, v157
	v_mul_f32_e32 v161, 0xbfb8aa3b, v161
	v_exp_f32_e32 v163, v161
	v_rcp_f32_e32 v161, v57
	v_add_f32_e32 v57, 1.0, v157
	v_lshlrev_b32_e32 v157, 16, v128
	v_rcp_f32_e32 v162, v57
	v_add_f32_e32 v57, 1.0, v163
	v_add_f32_e32 v157, v60, v157
	s_waitcnt vmcnt(14)
	v_lshlrev_b32_e32 v163, 16, v131
	v_mul_f32_e32 v157, 0xbfb8aa3b, v157
	v_add_f32_e32 v163, v60, v163
	v_exp_f32_e32 v157, v157
	v_mul_f32_e32 v163, 0xbfb8aa3b, v163
	v_exp_f32_e32 v165, v163
	v_rcp_f32_e32 v163, v57
	v_add_f32_e32 v57, 1.0, v157
	v_rcp_f32_e32 v164, v57
	v_add_f32_e32 v57, 1.0, v165
	v_rcp_f32_e32 v165, v57
	s_waitcnt lgkmcnt(7)
	v_add_f32_e32 v57, v141, v149
	s_waitcnt lgkmcnt(6)
	v_add_f32_e32 v141, v142, v150
	v_cndmask_b32_e64 v142, v156, 0, s[6:7]
	v_cndmask_b32_e64 v11, 0, v11, s[12:13]
	v_add_f32_e32 v11, v142, v11
	v_cndmask_b32_e64 v56, 0, v56, s[14:15]
	v_add_f32_e32 v11, v11, v56
	v_add_f32_e32 v57, 0x2b8cbccc, v57
	s_waitcnt lgkmcnt(5)
	v_add_f32_e32 v150, v143, v151
	s_waitcnt lgkmcnt(4)
	v_add_f32_e32 v151, v144, v152
	v_add_f32_e32 v56, v139, v11
	v_rsq_f32_e32 v144, v57
	v_add_f32_e32 v57, v138, v11
	v_mul_f32_e32 v56, 0x3fb8aa3b, v56
	v_mul_f32_e32 v57, 0x3fb8aa3b, v57
	v_exp_f32_e32 v56, v56
	v_exp_f32_e32 v57, v57
	v_add_f32_e32 v141, 0x2b8cbccc, v141
	s_waitcnt lgkmcnt(3)
	v_add_f32_e32 v152, v145, v153
	v_rsq_f32_e32 v145, v141
	v_mul_f32_e32 v139, 0x3fb8aa3b, v11
	s_waitcnt lgkmcnt(2)
	v_add_f32_e32 v153, v146, v154
	s_waitcnt lgkmcnt(1)
	v_add_f32_e32 v154, v147, v155
	s_waitcnt lgkmcnt(0)
	v_add_f32_e32 v155, v140, v148
	v_exp_f32_e32 v140, v139
	v_rcp_f32_e32 v142, v56
	v_rcp_f32_e32 v143, v57
	v_pk_add_f32 v[138:139], v[158:159], -1.0 op_sel_hi:[1,0]
	v_pk_mul_f32 v[52:53], v[52:53], v[144:145]
	v_pk_fma_f32 v[138:139], v[16:17], v[138:139], 1.0 op_sel_hi:[0,1,0]
	v_pk_mul_f32 v[144:145], v[158:159], v[52:53]
	v_mov_b32_e32 v141, v56
	v_lshlrev_b32_e32 v147, 16, v17
	v_lshlrev_b32_e32 v146, 16, v22
	v_pk_mul_f32 v[54:55], v[138:139], v[54:55]
	v_pk_mul_f32 v[138:139], v[10:11], v[142:143] op_sel_hi:[0,1]
	v_pk_mul_f32 v[52:53], v[140:141], v[52:53] neg_lo:[0,1] neg_hi:[0,1]
	v_pk_mul_f32 v[140:141], v[144:145], v[142:143]
	v_pk_mul_f32 v[146:147], v[56:57], v[146:147]
	v_pk_mul_f32 v[148:149], v[54:55], v[138:139]
	v_pk_mul_f32 v[54:55], v[54:55], v[142:143]
	v_pk_mul_f32 v[138:139], v[144:145], v[138:139]
	v_cvt_pk_bf16_f32 v52, v52, v53
	v_cvt_pk_bf16_f32 v53, v140, v141
	v_cvt_pk_bf16_f32 v54, v54, v55
	v_cvt_pk_bf16_f32 v55, v146, v147
	v_cvt_pk_bf16_f32 v56, v138, v139
	v_cvt_pk_bf16_f32 v138, v148, v149
	ds_write_b16 v101, v52
	ds_write_b16_d16_hi v101, v52 offset:144
	ds_write_b16 v101, v53 offset:4608
	ds_write_b16_d16_hi v101, v53 offset:4752
	ds_write_b16 v101, v54 offset:9216
	ds_write_b16_d16_hi v101, v54 offset:9360
	ds_write_b16 v101, v55 offset:13824
	ds_write_b16_d16_hi v101, v55 offset:13968
	ds_write_b16 v101, v56 offset:18432
	ds_write_b16_d16_hi v101, v56 offset:18576
	ds_write_b16 v101, v138 offset:23040
	v_add_f32_e32 v53, 0x2b8cbccc, v150
	v_add_f32_e32 v52, v136, v11
	v_rsq_f32_e32 v136, v53
	v_add_f32_e32 v53, v137, v11
	v_mul_f32_e32 v52, 0x3fb8aa3b, v52
	v_mul_f32_e32 v53, 0x3fb8aa3b, v53
	v_exp_f32_e32 v52, v52
	v_exp_f32_e32 v53, v53
	v_add_f32_e32 v56, 0x2b8cbccc, v151
	v_rsq_f32_e32 v137, v56
	v_rcp_f32_e32 v54, v52
	v_rcp_f32_e32 v55, v53
	ds_write_b16_d16_hi v101, v138 offset:23184
	ds_write_b16 v101, v69 offset:27648
	ds_write_b16 v101, v80 offset:27792
	v_pk_add_f32 v[138:139], v[160:161], -1.0 op_sel_hi:[1,0]
	v_pk_mul_f32 v[12:13], v[12:13], v[136:137]
	v_pk_fma_f32 v[138:139], v[16:17], v[138:139], 1.0 op_sel_hi:[0,1,0]
	v_pk_mul_f32 v[50:51], v[138:139], v[50:51]
	v_pk_mul_f32 v[138:139], v[10:11], v[54:55] op_sel_hi:[0,1]
	v_pk_mul_f32 v[136:137], v[160:161], v[12:13]
	v_mov_b32_e32 v56, v57
	v_mov_b32_e32 v57, v52
	v_lshlrev_b32_e32 v141, 16, v21
	v_lshlrev_b32_e32 v140, 16, v28
	v_pk_mul_f32 v[142:143], v[50:51], v[138:139]
	v_pk_mul_f32 v[50:51], v[50:51], v[54:55]
	v_pk_mul_f32 v[12:13], v[56:57], v[12:13] neg_lo:[0,1] neg_hi:[0,1]
	v_pk_mul_f32 v[54:55], v[136:137], v[54:55]
	v_pk_mul_f32 v[140:141], v[52:53], v[140:141]
	v_pk_mul_f32 v[56:57], v[136:137], v[138:139]
	v_cvt_pk_bf16_f32 v12, v12, v13
	v_cvt_pk_bf16_f32 v13, v54, v55
	v_cvt_pk_bf16_f32 v50, v50, v51
	v_cvt_pk_bf16_f32 v51, v140, v141
	v_cvt_pk_bf16_f32 v52, v56, v57
	v_cvt_pk_bf16_f32 v54, v142, v143
	ds_write_b16 v102, v12
	ds_write_b16_d16_hi v102, v12 offset:144
	ds_write_b16 v102, v13 offset:4608
	ds_write_b16_d16_hi v102, v13 offset:4752
	ds_write_b16 v102, v50 offset:9216
	ds_write_b16_d16_hi v102, v50 offset:9360
	ds_write_b16 v102, v51 offset:13824
	ds_write_b16_d16_hi v102, v51 offset:13968
	ds_write_b16 v102, v52 offset:18432
	ds_write_b16_d16_hi v102, v52 offset:18576
	ds_write_b16 v102, v54 offset:23040
	v_add_f32_e32 v13, 0x2b8cbccc, v152
	v_add_f32_e32 v12, v135, v11
	ds_write_b16_d16_hi v102, v54 offset:23184
	ds_write_b16 v102, v85 offset:27648
	ds_write_b16 v102, v88 offset:27792
	v_rsq_f32_e32 v54, v13
	v_add_f32_e32 v13, v134, v11
	v_mul_f32_e32 v12, 0x3fb8aa3b, v12
	v_mul_f32_e32 v13, 0x3fb8aa3b, v13
	v_exp_f32_e32 v12, v12
	v_exp_f32_e32 v13, v13
	v_add_f32_e32 v52, 0x2b8cbccc, v153
	v_rsq_f32_e32 v55, v52
	v_rcp_f32_e32 v50, v12
	v_rcp_f32_e32 v51, v13
	v_pk_add_f32 v[56:57], v[162:163], -1.0 op_sel_hi:[1,0]
	v_pk_mul_f32 v[6:7], v[6:7], v[54:55]
	v_pk_fma_f32 v[56:57], v[16:17], v[56:57], 1.0 op_sel_hi:[0,1,0]
	v_pk_mul_f32 v[8:9], v[56:57], v[8:9]
	v_pk_mul_f32 v[56:57], v[10:11], v[50:51] op_sel_hi:[0,1]
	v_pk_mul_f32 v[54:55], v[162:163], v[6:7]
	v_mov_b32_e32 v52, v53
	v_mov_b32_e32 v53, v12
	v_lshlrev_b32_e32 v135, 16, v25
	v_lshlrev_b32_e32 v134, 16, v32
	v_pk_mul_f32 v[136:137], v[8:9], v[56:57]
	v_pk_mul_f32 v[8:9], v[8:9], v[50:51]
	v_pk_mul_f32 v[6:7], v[52:53], v[6:7] neg_lo:[0,1] neg_hi:[0,1]
	v_pk_mul_f32 v[50:51], v[54:55], v[50:51]
	v_pk_mul_f32 v[134:135], v[12:13], v[134:135]
	v_pk_mul_f32 v[52:53], v[54:55], v[56:57]
	v_cvt_pk_bf16_f32 v6, v6, v7
	v_cvt_pk_bf16_f32 v7, v50, v51
	v_cvt_pk_bf16_f32 v8, v8, v9
	v_cvt_pk_bf16_f32 v9, v134, v135
	v_cvt_pk_bf16_f32 v12, v52, v53
	v_cvt_pk_bf16_f32 v50, v136, v137
	ds_write_b16 v103, v6
	ds_write_b16_d16_hi v103, v6 offset:144
	ds_write_b16 v103, v7 offset:4608
	ds_write_b16_d16_hi v103, v7 offset:4752
	ds_write_b16 v103, v8 offset:9216
	ds_write_b16_d16_hi v103, v8 offset:9360
	ds_write_b16 v103, v9 offset:13824
	ds_write_b16_d16_hi v103, v9 offset:13968
	ds_write_b16 v103, v12 offset:18432
	ds_write_b16_d16_hi v103, v12 offset:18576
	ds_write_b16 v103, v50 offset:23040
	v_add_f32_e32 v7, 0x2b8cbccc, v154
	v_add_f32_e32 v6, v133, v11
	ds_write_b16_d16_hi v103, v50 offset:23184
	ds_write_b16 v103, v107 offset:27648
	ds_write_b16 v103, v118 offset:27792
	v_rsq_f32_e32 v50, v7
	v_add_f32_e32 v7, v14, v11
	v_mul_f32_e32 v6, 0x3fb8aa3b, v6
	v_mul_f32_e32 v7, 0x3fb8aa3b, v7
	v_exp_f32_e32 v6, v6
	v_exp_f32_e32 v7, v7
	v_add_f32_e32 v11, 0x2b8cbccc, v155
	v_rsq_f32_e32 v51, v11
	v_rcp_f32_e32 v8, v6
	v_rcp_f32_e32 v9, v7
	v_pk_add_f32 v[52:53], v[164:165], -1.0 op_sel_hi:[1,0]
	s_add_i32 s55, s50, s52
	v_pk_fma_f32 v[52:53], v[16:17], v[52:53], 1.0 op_sel_hi:[0,1,0]
	v_pk_mul_f32 v[2:3], v[2:3], v[50:51]
	v_mov_b32_e32 v12, v13
	v_mov_b32_e32 v13, v6
	s_cmpk_gt_i32 s55, 0x1fff
	s_waitcnt vmcnt(13)
	v_lshlrev_b32_e32 v55, 16, v31
	v_lshlrev_b32_e32 v54, 16, v48
	v_pk_mul_f32 v[4:5], v[52:53], v[4:5]
	v_pk_mul_f32 v[10:11], v[10:11], v[8:9] op_sel_hi:[0,1]
	v_pk_mul_f32 v[50:51], v[164:165], v[2:3]
	v_pk_mul_f32 v[2:3], v[12:13], v[2:3] neg_lo:[0,1] neg_hi:[0,1]
	s_cselect_b64 s[0:1], -1, 0
	v_pk_mul_f32 v[54:55], v[6:7], v[54:55]
	v_pk_mul_f32 v[52:53], v[4:5], v[10:11]
	v_pk_mul_f32 v[4:5], v[4:5], v[8:9]
	v_pk_mul_f32 v[6:7], v[50:51], v[8:9]
	v_pk_mul_f32 v[8:9], v[50:51], v[10:11]
	v_cvt_pk_bf16_f32 v2, v2, v3
	s_and_b64 vcc, exec, s[0:1]
	v_cvt_pk_bf16_f32 v3, v6, v7
	v_cvt_pk_bf16_f32 v4, v4, v5
	v_cvt_pk_bf16_f32 v5, v54, v55
	v_cvt_pk_bf16_f32 v6, v8, v9
	v_cvt_pk_bf16_f32 v7, v52, v53
	ds_write_b16 v104, v2
	ds_write_b16_d16_hi v104, v2 offset:144
	ds_write_b16 v104, v3 offset:4608
	ds_write_b16_d16_hi v104, v3 offset:4752
	ds_write_b16 v104, v4 offset:9216
	ds_write_b16_d16_hi v104, v4 offset:9360
	ds_write_b16 v104, v5 offset:13824
	ds_write_b16_d16_hi v104, v5 offset:13968
	ds_write_b16 v104, v6 offset:18432
	ds_write_b16_d16_hi v104, v6 offset:18576
	ds_write_b16 v104, v7 offset:23040
	ds_write_b16_d16_hi v104, v7 offset:23184
	ds_write_b16 v104, v129 offset:27648
	s_waitcnt vmcnt(12)
	ds_write_b16 v104, v132 offset:27792
	s_cbranch_vccnz .LBB0_3541
	s_add_i32 s2, s54, s50
	s_ashr_i32 s3, s2, 31
	s_lshr_b32 s3, s3, 25
	s_add_i32 s3, s2, s3
	s_ashr_i32 s50, s3, 7
	s_and_b32 s3, s3, 0x7ffff80
	s_sub_i32 s2, s2, s3
	s_lshl_b32 s49, s50, 8
	s_and_b32 s3, s50, 1
	s_and_b32 s49, s49, 0x7ff000
	s_lshl_b32 s2, s2, 5
	s_lshl_b32 s50, s50, 5
	s_add_i32 s49, s49, s2
	s_lshl_b32 s2, s3, 9
	s_and_b32 s50, s50, 0x1c0
	s_or_b32 s2, s2, s50
	v_or_b32_e32 v1, s2, v33
	v_lshlrev_b32_e32 v1, 2, v1
	v_or_b32_e32 v6, s50, v33
	s_cmp_eq_u32 s3, 0
	global_load_dword v59, v1, s[4:5]
	global_load_dword v60, v1, s[30:31]
	v_lshlrev_b32_e32 v1, 2, v6
	s_cselect_b64 vcc, -1, 0
	global_load_dword v16, v1, s[36:37]
	global_load_dword v18, v1, s[34:35]
	v_cndmask_b32_e32 v1, v58, v49, vcc
	v_or_b32_e32 v1, s49, v1
	v_lshl_or_b32 v14, v1, 9, v6
	v_lshlrev_b64 v[2:3], 1, v[14:15]
	v_lshl_add_u64 v[4:5], s[40:41], 0, v[2:3]
	global_load_ushort v20, v[4:5], off
	v_lshl_add_u64 v[4:5], s[44:45], 0, v[2:3]
	v_cndmask_b32_e32 v1, v62, v61, vcc
	global_load_ushort v67, v[4:5], off
	v_lshl_add_u64 v[4:5], s[46:47], 0, v[2:3]
	v_or_b32_e32 v1, s49, v1
	global_load_ushort v68, v[4:5], off
	v_lshl_add_u64 v[4:5], s[38:39], 0, v[2:3]
	v_lshl_add_u64 v[2:3], s[42:43], 0, v[2:3]
	v_lshl_or_b32 v14, v1, 9, v6
	global_load_ushort v22, v[4:5], off
	global_load_ushort v69, v[2:3], off
	v_lshlrev_b64 v[2:3], 1, v[14:15]
	v_lshl_add_u64 v[4:5], s[40:41], 0, v[2:3]
	global_load_ushort v1, v[4:5], off
	v_lshl_add_u64 v[4:5], s[44:45], 0, v[2:3]
	global_load_ushort v72, v[4:5], off
	v_lshl_add_u64 v[4:5], s[46:47], 0, v[2:3]
	global_load_ushort v75, v[4:5], off
	v_lshl_add_u64 v[4:5], s[38:39], 0, v[2:3]
	v_lshl_add_u64 v[2:3], s[42:43], 0, v[2:3]
	global_load_ushort v17, v[4:5], off
	global_load_ushort v80, v[2:3], off
	v_cndmask_b32_e32 v2, v64, v63, vcc
	v_or_b32_e32 v2, s49, v2
	v_lshl_or_b32 v14, v2, 9, v6
	v_lshlrev_b64 v[2:3], 1, v[14:15]
	v_lshl_add_u64 v[4:5], s[40:41], 0, v[2:3]
	global_load_ushort v24, v[4:5], off
	v_lshl_add_u64 v[4:5], s[44:45], 0, v[2:3]
	global_load_ushort v81, v[4:5], off
	v_lshl_add_u64 v[4:5], s[46:47], 0, v[2:3]
	global_load_ushort v84, v[4:5], off
	v_lshl_add_u64 v[4:5], s[38:39], 0, v[2:3]
	v_lshl_add_u64 v[2:3], s[42:43], 0, v[2:3]
	global_load_ushort v28, v[4:5], off
	global_load_ushort v85, v[2:3], off
	v_cndmask_b32_e32 v2, v66, v65, vcc
	v_or_b32_e32 v2, s49, v2
	v_lshl_or_b32 v14, v2, 9, v6
	v_lshlrev_b64 v[2:3], 1, v[14:15]
	v_lshl_add_u64 v[4:5], s[40:41], 0, v[2:3]
	global_load_ushort v19, v[4:5], off
	v_lshl_add_u64 v[4:5], s[44:45], 0, v[2:3]
	global_load_ushort v86, v[4:5], off
	v_lshl_add_u64 v[4:5], s[46:47], 0, v[2:3]
	global_load_ushort v87, v[4:5], off
	v_lshl_add_u64 v[4:5], s[38:39], 0, v[2:3]
	v_lshl_add_u64 v[2:3], s[42:43], 0, v[2:3]
	global_load_ushort v21, v[4:5], off
	global_load_ushort v88, v[2:3], off
	v_cndmask_b32_e32 v2, v71, v70, vcc
	v_or_b32_e32 v2, s49, v2
	v_lshl_or_b32 v14, v2, 9, v6
	v_lshlrev_b64 v[2:3], 1, v[14:15]
	v_lshl_add_u64 v[4:5], s[40:41], 0, v[2:3]
	global_load_ushort v30, v[4:5], off
	v_lshl_add_u64 v[4:5], s[44:45], 0, v[2:3]
	global_load_ushort v96, v[4:5], off
	v_lshl_add_u64 v[4:5], s[46:47], 0, v[2:3]
	global_load_ushort v100, v[4:5], off
	v_lshl_add_u64 v[4:5], s[38:39], 0, v[2:3]
	v_lshl_add_u64 v[2:3], s[42:43], 0, v[2:3]
	global_load_ushort v32, v[4:5], off
	global_load_ushort v107, v[2:3], off
	v_cndmask_b32_e32 v2, v74, v73, vcc
	v_or_b32_e32 v2, s49, v2
	v_lshl_or_b32 v14, v2, 9, v6
	v_lshlrev_b64 v[2:3], 1, v[14:15]
	v_lshl_add_u64 v[4:5], s[40:41], 0, v[2:3]
	global_load_ushort v23, v[4:5], off
	v_lshl_add_u64 v[4:5], s[44:45], 0, v[2:3]
	global_load_ushort v113, v[4:5], off
	v_lshl_add_u64 v[4:5], s[46:47], 0, v[2:3]
	global_load_ushort v114, v[4:5], off
	v_lshl_add_u64 v[4:5], s[38:39], 0, v[2:3]
	v_lshl_add_u64 v[2:3], s[42:43], 0, v[2:3]
	global_load_ushort v25, v[4:5], off
	global_load_ushort v118, v[2:3], off
	v_cndmask_b32_e32 v2, v77, v76, vcc
	v_or_b32_e32 v2, s49, v2
	v_lshl_or_b32 v14, v2, 9, v6
	v_lshlrev_b64 v[2:3], 1, v[14:15]
	v_lshl_add_u64 v[4:5], s[40:41], 0, v[2:3]
	global_load_ushort v46, v[4:5], off
	v_lshl_add_u64 v[4:5], s[44:45], 0, v[2:3]
	global_load_ushort v127, v[4:5], off
	v_lshl_add_u64 v[4:5], s[46:47], 0, v[2:3]
	global_load_ushort v128, v[4:5], off
	v_lshl_add_u64 v[4:5], s[38:39], 0, v[2:3]
	v_lshl_add_u64 v[2:3], s[42:43], 0, v[2:3]
	global_load_ushort v48, v[4:5], off
	global_load_ushort v129, v[2:3], off
	v_cndmask_b32_e32 v2, v79, v78, vcc
	v_or_b32_e32 v2, s49, v2
	v_lshl_or_b32 v14, v2, 9, v6
	v_lshlrev_b64 v[2:3], 1, v[14:15]
	v_lshl_add_u64 v[4:5], s[40:41], 0, v[2:3]
	global_load_ushort v29, v[4:5], off
	v_lshl_add_u64 v[4:5], s[44:45], 0, v[2:3]
	global_load_ushort v130, v[4:5], off
	v_lshl_add_u64 v[4:5], s[46:47], 0, v[2:3]
	global_load_ushort v131, v[4:5], off
	v_lshl_add_u64 v[4:5], s[38:39], 0, v[2:3]
	v_lshl_add_u64 v[2:3], s[42:43], 0, v[2:3]
	global_load_ushort v31, v[4:5], off
	global_load_ushort v132, v[2:3], off
